# s_setprio 1 moved ahead of the pre-MMA barrier in the expert GEMM K loops (priority raised before the rendezvous)
# speedup vs baseline: 1.0021x; 1.0021x over previous
; #define PG8_STAGEB(bufoff, gbase) glds2(voffB, (gbase), voffB, (gbase) + qstep, ldsb + (bufoff))
; #define PG8_STAGEA(bufoff, rowb, v, h, kb) do { if constexpr (GATHER) glds2((v)[h][0], Ab + (kb), (v)[h][1], Ab + (kb), ldsb + (bufoff)); \
;         else glds2(voffA, Ab + (rowb) + (h) * hstep + (kb), voffA, Ab + (rowb) + (h) * hstep + qstep + (kb), ldsb + (bufoff)); } while (0)
; #define PG8_LDA(dst, b, h) do { _Pragma("unroll") for (int m = 0; m < 4; ++m) _Pragma("unroll") for (int k = 0; k < 2; ++k) dst[m][k] = *(const PG8_LAS bf16x8*)(lds + PG8_SA(b, h) + aoff + m * 2048 + k * 1024); } while (0)
; #define PG8_LDB(dst, b, h) do { _Pragma("unroll") for (int n = 0; n < 2; ++n) _Pragma("unroll") for (int k = 0; k < 2; ++k) dst[n][k] = *(const PG8_LAS bf16x8*)(lds + PG8_SB(b, h) + boff + n * 2048 + k * 1024); } while (0)
; #define PG8_WAIT_V(n) asm volatile("s_waitcnt vmcnt(" #n ")" ::: "memory")
; #define PG8_WAIT_L(n) asm volatile("s_waitcnt lgkmcnt(" #n ")" ::: "memory")
; #define PG8_BAR __builtin_amdgcn_s_barrier()
; #define PG8_SCHED __builtin_amdgcn_sched_barrier(0)
; template <class Epi, bool GATHER, int MODE, bool SPLIT = false>
; __device__ __forceinline__ void gemm_phase(PG8_LAS unsigned char* lds, const Gemm g, const Order& S, const Epi& E) {
;     ...
;             PG8_LDB(B0, 0, 0); PG8_LDB(B1, 0, 1); PG8_SCHED; PG8_LDA(At, 0, 0); PG8_STAGEA(PG8_SA(1, 1), cAr, cv, 1, k1);
;             PG8_WAIT_V(8); PG8_WAIT_L(0); PG8_BAR; PG8_MMA(0, 0, At, B0); PG8_MMA(0, 1, At, B1); PG8_BAR; PG8_SCHED;
;             PG8_LDA(At, 0, 1); PG8_STAGEB(PG8_SB(0, 0), b2); PG8_STAGEB(PG8_SB(0, 1), b2 + hstep); PG8_STAGEA(PG8_SA(0, 0), cAr, cv, 0, k2);
;             PG8_WAIT_V(8); PG8_WAIT_L(0); PG8_BAR; PG8_MMA(1, 0, At, B0); PG8_MMA(1, 1, At, B1); PG8_BAR; PG8_SCHED;
;             PG8_LDB(B0, 1, 0); PG8_LDB(B1, 1, 1); PG8_SCHED; PG8_LDA(At, 1, 0); PG8_STAGEA(PG8_SA(0, 1), cAr, cv, 1, k2);
;             PG8_WAIT_V(8); PG8_WAIT_L(0); PG8_BAR; PG8_MMA(0, 0, At, B0); PG8_MMA(0, 1, At, B1); PG8_BAR; PG8_SCHED;
.LBB0_802:
	ds_read_b128 v[158:161], v179
	ds_read_b128 v[150:153], v179 offset:1024
	ds_read_b128 v[154:157], v179 offset:2048
	ds_read_b128 v[146:149], v179 offset:3072
	ds_read_b128 v[142:145], v180
	ds_read_b128 v[130:133], v180 offset:1024
	ds_read_b128 v[138:141], v180 offset:2048
	ds_read_b128 v[134:137], v180 offset:3072
	s_add_u32 s66, s34, s30
	s_addc_u32 s67, s35, s31
	s_add_u32 s36, s66, 0x100
	s_addc_u32 s37, s67, 0
	ds_read_b128 v[194:197], v181
	ds_read_b128 v[198:201], v181 offset:1024
	ds_read_b128 v[202:205], v181 offset:2048
	ds_read_b128 v[206:209], v181 offset:3072
	ds_read_b128 v[210:213], v181 offset:4096
	ds_read_b128 v[214:217], v181 offset:5120
	ds_read_b128 v[218:221], v181 offset:6144
	ds_read_b128 v[222:225], v181 offset:7168
	s_add_u32 s27, s6, s30
	s_addc_u32 s29, s7, s31
	s_add_u32 s68, s27, 0x80
	s_addc_u32 s69, s29, 0
	s_mov_b32 s70, m0
	s_mov_b32 m0, s62
	s_nop 0
	global_load_lds_dwordx4 v189, s[68:69]
	s_mov_b32 m0, s63
	s_nop 0
	global_load_lds_dwordx4 v190, s[68:69]
	s_mov_b32 m0, s70
	s_waitcnt vmcnt(8)
	s_waitcnt lgkmcnt(0)
	s_setprio 1
	s_barrier
	s_waitcnt lgkmcnt(7)
	v_mfma_i32_16x16x64_i8 v[126:129], v[158:161], v[194:197], v[126:129]
	v_mfma_i32_16x16x64_i8 v[122:125], v[154:157], v[194:197], v[122:125]
	s_waitcnt lgkmcnt(5)
	v_mfma_i32_16x16x64_i8 v[118:121], v[158:161], v[202:205], v[118:121]
	v_mfma_i32_16x16x64_i8 v[106:109], v[154:157], v[202:205], v[106:109]
	s_waitcnt lgkmcnt(3)
	v_mfma_i32_16x16x64_i8 v[102:105], v[158:161], v[210:213], v[102:105]
	v_mfma_i32_16x16x64_i8 v[90:93], v[154:157], v[210:213], v[90:93]
	s_waitcnt lgkmcnt(1)
	v_mfma_i32_16x16x64_i8 v[86:89], v[158:161], v[218:221], v[86:89]
	v_mfma_i32_16x16x64_i8 v[74:77], v[154:157], v[218:221], v[74:77]
	v_mfma_i32_16x16x64_i8 v[126:129], v[150:153], v[198:201], v[126:129]
	v_mfma_i32_16x16x64_i8 v[122:125], v[146:149], v[198:201], v[122:125]
	v_mfma_i32_16x16x64_i8 v[118:121], v[150:153], v[206:209], v[118:121]
	v_mfma_i32_16x16x64_i8 v[106:109], v[146:149], v[206:209], v[106:109]
	v_mfma_i32_16x16x64_i8 v[102:105], v[150:153], v[214:217], v[102:105]
	v_mfma_i32_16x16x64_i8 v[90:93], v[146:149], v[214:217], v[90:93]
	s_waitcnt lgkmcnt(0)
	v_mfma_i32_16x16x64_i8 v[86:89], v[150:153], v[222:225], v[86:89]
	v_mfma_i32_16x16x64_i8 v[74:77], v[146:149], v[222:225], v[74:77]
	s_setprio 0
	s_setprio 1
	v_mfma_i32_16x16x64_i8 v[114:117], v[142:145], v[194:197], v[114:117]
	v_mfma_i32_16x16x64_i8 v[110:113], v[138:141], v[194:197], v[110:113]
	v_mfma_i32_16x16x64_i8 v[98:101], v[142:145], v[202:205], v[98:101]
	v_mfma_i32_16x16x64_i8 v[94:97], v[138:141], v[202:205], v[94:97]
	v_mfma_i32_16x16x64_i8 v[82:85], v[142:145], v[210:213], v[82:85]
	v_mfma_i32_16x16x64_i8 v[78:81], v[138:141], v[210:213], v[78:81]
	v_mfma_i32_16x16x64_i8 v[70:73], v[142:145], v[218:221], v[70:73]
	v_mfma_i32_16x16x64_i8 v[66:69], v[138:141], v[218:221], v[66:69]
	s_nop 0
	v_mfma_i32_16x16x64_i8 v[114:117], v[130:133], v[198:201], v[114:117]
	v_mfma_i32_16x16x64_i8 v[110:113], v[134:137], v[198:201], v[110:113]
	v_mfma_i32_16x16x64_i8 v[98:101], v[130:133], v[206:209], v[98:101]
	v_mfma_i32_16x16x64_i8 v[94:97], v[134:137], v[206:209], v[94:97]
	v_mfma_i32_16x16x64_i8 v[82:85], v[130:133], v[214:217], v[82:85]
	v_mfma_i32_16x16x64_i8 v[78:81], v[134:137], v[214:217], v[78:81]
	v_mfma_i32_16x16x64_i8 v[70:73], v[130:133], v[222:225], v[70:73]
	v_mfma_i32_16x16x64_i8 v[66:69], v[134:137], v[222:225], v[66:69]
	s_setprio 0
	s_barrier
	s_add_u32 s68, s66, 0x20100
	s_addc_u32 s69, s67, 0
	ds_read_b128 v[194:197], v181 offset:16384
	ds_read_b128 v[198:201], v181 offset:17408
	ds_read_b128 v[202:205], v181 offset:18432
	ds_read_b128 v[206:209], v181 offset:19456
	ds_read_b128 v[210:213], v181 offset:20480
	ds_read_b128 v[214:217], v181 offset:21504
	ds_read_b128 v[218:221], v181 offset:22528
	ds_read_b128 v[222:225], v181 offset:23552
	s_mov_b32 s70, m0
	s_mov_b32 m0, s49
	s_nop 0
	global_load_lds_dwordx4 v168, s[36:37]
	s_mov_b32 m0, s50
	s_nop 0
	global_load_lds_dwordx4 v168, s[68:69]
	s_mov_b32 m0, s70
	s_add_u32 s36, s66, 0x40100
	s_addc_u32 s37, s67, 0
	s_add_u32 s68, s66, 0x60100
	s_addc_u32 s69, s67, 0
	s_mov_b32 s70, m0
	s_mov_b32 m0, s51
	s_nop 0
	global_load_lds_dwordx4 v168, s[36:37]
	s_mov_b32 m0, s52
	s_nop 0
	global_load_lds_dwordx4 v168, s[68:69]
	s_mov_b32 m0, s70
	s_add_u32 s36, s27, 0x100
	s_addc_u32 s37, s29, 0
	s_mov_b32 s68, m0
	s_mov_b32 m0, s43
	s_nop 0
	global_load_lds_dwordx4 v191, s[36:37]
	s_mov_b32 m0, s53
	s_nop 0
	global_load_lds_dwordx4 v192, s[36:37]
	s_mov_b32 m0, s68
	s_waitcnt vmcnt(8)
	s_waitcnt lgkmcnt(0)
	s_setprio 1
	s_barrier
; #define PG8_STAGEB(bufoff, gbase) glds2(voffB, (gbase), voffB, (gbase) + qstep, ldsb + (bufoff))
; #define PG8_STAGEA(bufoff, rowb, v, h, kb) do { if constexpr (GATHER) glds2((v)[h][0], Ab + (kb), (v)[h][1], Ab + (kb), ldsb + (bufoff)); \
;         else glds2(voffA, Ab + (rowb) + (h) * hstep + (kb), voffA, Ab + (rowb) + (h) * hstep + qstep + (kb), ldsb + (bufoff)); } while (0)
; #define PG8_LDA(dst, b, h) do { _Pragma("unroll") for (int m = 0; m < 4; ++m) _Pragma("unroll") for (int k = 0; k < 2; ++k) dst[m][k] = *(const PG8_LAS bf16x8*)(lds + PG8_SA(b, h) + aoff + m * 2048 + k * 1024); } while (0)
; #define PG8_LDB(dst, b, h) do { _Pragma("unroll") for (int n = 0; n < 2; ++n) _Pragma("unroll") for (int k = 0; k < 2; ++k) dst[n][k] = *(const PG8_LAS bf16x8*)(lds + PG8_SB(b, h) + boff + n * 2048 + k * 1024); } while (0)
; #define PG8_WAIT_V(n) asm volatile("s_waitcnt vmcnt(" #n ")" ::: "memory")
; #define PG8_WAIT_L(n) asm volatile("s_waitcnt lgkmcnt(" #n ")" ::: "memory")
; #define PG8_BAR __builtin_amdgcn_s_barrier()
; #define PG8_SCHED __builtin_amdgcn_sched_barrier(0)
; template <class Epi, bool GATHER, int MODE, bool SPLIT = false>
; __device__ __forceinline__ void gemm_phase(PG8_LAS unsigned char* lds, const Gemm g, const Order& S, const Epi& E) {
;     ...
;             PG8_WAIT_V(8); PG8_WAIT_L(0); PG8_BAR; PG8_MMA(1, 0, At, B0); PG8_MMA(1, 1, At, B1); PG8_BAR; PG8_SCHED;
;             PG8_LDB(B0, 1, 0); PG8_LDB(B1, 1, 1); PG8_SCHED; PG8_LDA(At, 1, 0); PG8_STAGEA(PG8_SA(0, 1), cAr, cv, 1, k2);
;             PG8_WAIT_V(8); PG8_WAIT_L(0); PG8_BAR; PG8_MMA(0, 0, At, B0); PG8_MMA(0, 1, At, B1); PG8_BAR; PG8_SCHED;
;             PG8_LDA(At, 1, 1); PG8_STAGEB(PG8_SB(1, 0), b3); PG8_STAGEB(PG8_SB(1, 1), b3 + hstep); PG8_STAGEA(PG8_SA(1, 0), cAr, cv, 0, k3);
	s_waitcnt lgkmcnt(7)
	v_mfma_i32_16x16x64_i8 v[62:65], v[158:161], v[194:197], v[62:65]
	v_mfma_i32_16x16x64_i8 v[58:61], v[154:157], v[194:197], v[58:61]
	s_waitcnt lgkmcnt(5)
	v_mfma_i32_16x16x64_i8 v[46:49], v[158:161], v[202:205], v[46:49]
	v_mfma_i32_16x16x64_i8 v[42:45], v[154:157], v[202:205], v[42:45]
	s_waitcnt lgkmcnt(3)
	v_mfma_i32_16x16x64_i8 v[38:41], v[158:161], v[210:213], v[38:41]
	v_mfma_i32_16x16x64_i8 v[34:37], v[154:157], v[210:213], v[34:37]
	s_waitcnt lgkmcnt(1)
	v_mfma_i32_16x16x64_i8 v[22:25], v[158:161], v[218:221], v[22:25]
	v_mfma_i32_16x16x64_i8 v[18:21], v[154:157], v[218:221], v[18:21]
	v_mfma_i32_16x16x64_i8 v[62:65], v[150:153], v[198:201], v[62:65]
	v_mfma_i32_16x16x64_i8 v[58:61], v[146:149], v[198:201], v[58:61]
	v_mfma_i32_16x16x64_i8 v[46:49], v[150:153], v[206:209], v[46:49]
	v_mfma_i32_16x16x64_i8 v[42:45], v[146:149], v[206:209], v[42:45]
	v_mfma_i32_16x16x64_i8 v[38:41], v[150:153], v[214:217], v[38:41]
	v_mfma_i32_16x16x64_i8 v[34:37], v[146:149], v[214:217], v[34:37]
	s_waitcnt lgkmcnt(0)
	v_mfma_i32_16x16x64_i8 v[22:25], v[150:153], v[222:225], v[22:25]
	v_mfma_i32_16x16x64_i8 v[18:21], v[146:149], v[222:225], v[18:21]
	s_setprio 0
	s_setprio 1
	v_mfma_i32_16x16x64_i8 v[54:57], v[142:145], v[194:197], v[54:57]
	v_mfma_i32_16x16x64_i8 v[50:53], v[138:141], v[194:197], v[50:53]
	v_mfma_i32_16x16x64_i8 v[30:33], v[142:145], v[202:205], v[30:33]
	v_mfma_i32_16x16x64_i8 v[26:29], v[138:141], v[202:205], v[26:29]
	v_mfma_i32_16x16x64_i8 v[14:17], v[142:145], v[210:213], v[14:17]
	v_mfma_i32_16x16x64_i8 v[10:13], v[138:141], v[210:213], v[10:13]
	v_mfma_i32_16x16x64_i8 v[6:9], v[142:145], v[218:221], v[6:9]
	v_mfma_i32_16x16x64_i8 v[2:5], v[138:141], v[218:221], v[2:5]
	s_nop 0
	v_mfma_i32_16x16x64_i8 v[54:57], v[130:133], v[198:201], v[54:57]
	v_mfma_i32_16x16x64_i8 v[50:53], v[134:137], v[198:201], v[50:53]
	v_mfma_i32_16x16x64_i8 v[30:33], v[130:133], v[206:209], v[30:33]
	v_mfma_i32_16x16x64_i8 v[26:29], v[134:137], v[206:209], v[26:29]
	v_mfma_i32_16x16x64_i8 v[14:17], v[130:133], v[214:217], v[14:17]
	v_mfma_i32_16x16x64_i8 v[10:13], v[134:137], v[214:217], v[10:13]
	v_mfma_i32_16x16x64_i8 v[6:9], v[130:133], v[222:225], v[6:9]
	v_mfma_i32_16x16x64_i8 v[2:5], v[134:137], v[222:225], v[2:5]
	s_setprio 0
	s_barrier
	v_add_u32_e32 v138, 0x1c000, v178
	ds_read_b128 v[130:133], v182
	ds_read_b128 v[134:137], v182 offset:1024
	ds_read_b128 v[140:143], v182 offset:2048
	ds_read_b128 v[144:147], v182 offset:3072
	ds_read_b128 v[148:151], v138
	ds_read_b128 v[152:155], v138 offset:1024
	ds_read_b128 v[156:159], v138 offset:2048
	ds_read_b128 v[194:197], v138 offset:3072
	ds_read_b128 v[198:201], v181 offset:32768
	ds_read_b128 v[202:205], v181 offset:33792
	ds_read_b128 v[206:209], v181 offset:34816
	ds_read_b128 v[210:213], v181 offset:35840
	ds_read_b128 v[214:217], v181 offset:36864
	ds_read_b128 v[218:221], v181 offset:37888
	ds_read_b128 v[222:225], v181 offset:38912
	ds_read_b128 v[226:229], v181 offset:39936
	s_mov_b32 s68, m0
	s_mov_b32 m0, s54
	s_nop 0
	global_load_lds_dwordx4 v189, s[36:37]
	s_mov_b32 m0, s55
	s_nop 0
	global_load_lds_dwordx4 v190, s[36:37]
	s_mov_b32 m0, s68
	s_waitcnt vmcnt(8)
	s_waitcnt lgkmcnt(0)
	s_setprio 1
	s_barrier
	s_waitcnt lgkmcnt(7)
	v_mfma_i32_16x16x64_i8 v[126:129], v[130:133], v[198:201], v[126:129]
	v_mfma_i32_16x16x64_i8 v[122:125], v[140:143], v[198:201], v[122:125]
	s_waitcnt lgkmcnt(5)
	v_mfma_i32_16x16x64_i8 v[118:121], v[130:133], v[206:209], v[118:121]
	v_mfma_i32_16x16x64_i8 v[106:109], v[140:143], v[206:209], v[106:109]
	s_waitcnt lgkmcnt(3)
	v_mfma_i32_16x16x64_i8 v[102:105], v[130:133], v[214:217], v[102:105]
	v_mfma_i32_16x16x64_i8 v[90:93], v[140:143], v[214:217], v[90:93]
	s_waitcnt lgkmcnt(1)
	v_mfma_i32_16x16x64_i8 v[86:89], v[130:133], v[222:225], v[86:89]
	v_mfma_i32_16x16x64_i8 v[74:77], v[140:143], v[222:225], v[74:77]
	v_mfma_i32_16x16x64_i8 v[126:129], v[134:137], v[202:205], v[126:129]
	v_mfma_i32_16x16x64_i8 v[122:125], v[144:147], v[202:205], v[122:125]
	v_mfma_i32_16x16x64_i8 v[118:121], v[134:137], v[210:213], v[118:121]
	v_mfma_i32_16x16x64_i8 v[106:109], v[144:147], v[210:213], v[106:109]
	v_mfma_i32_16x16x64_i8 v[102:105], v[134:137], v[218:221], v[102:105]
	v_mfma_i32_16x16x64_i8 v[90:93], v[144:147], v[218:221], v[90:93]
	s_waitcnt lgkmcnt(0)
	v_mfma_i32_16x16x64_i8 v[86:89], v[134:137], v[226:229], v[86:89]
	v_mfma_i32_16x16x64_i8 v[74:77], v[144:147], v[226:229], v[74:77]
	s_setprio 0
	s_setprio 1
	v_mfma_i32_16x16x64_i8 v[114:117], v[148:151], v[198:201], v[114:117]
	v_mfma_i32_16x16x64_i8 v[110:113], v[156:159], v[198:201], v[110:113]
	v_mfma_i32_16x16x64_i8 v[98:101], v[148:151], v[206:209], v[98:101]
	v_mfma_i32_16x16x64_i8 v[94:97], v[156:159], v[206:209], v[94:97]
	v_mfma_i32_16x16x64_i8 v[82:85], v[148:151], v[214:217], v[82:85]
	v_mfma_i32_16x16x64_i8 v[78:81], v[156:159], v[214:217], v[78:81]
	v_mfma_i32_16x16x64_i8 v[70:73], v[148:151], v[222:225], v[70:73]
	v_mfma_i32_16x16x64_i8 v[66:69], v[156:159], v[222:225], v[66:69]
	s_nop 0
	v_mfma_i32_16x16x64_i8 v[114:117], v[152:155], v[202:205], v[114:117]
	v_mfma_i32_16x16x64_i8 v[110:113], v[194:197], v[202:205], v[110:113]
	v_mfma_i32_16x16x64_i8 v[98:101], v[152:155], v[210:213], v[98:101]
	v_mfma_i32_16x16x64_i8 v[94:97], v[194:197], v[210:213], v[94:97]
	v_mfma_i32_16x16x64_i8 v[82:85], v[152:155], v[218:221], v[82:85]
	v_mfma_i32_16x16x64_i8 v[78:81], v[194:197], v[218:221], v[78:81]
	v_mfma_i32_16x16x64_i8 v[70:73], v[152:155], v[226:229], v[70:73]
	v_mfma_i32_16x16x64_i8 v[66:69], v[194:197], v[226:229], v[66:69]
	s_setprio 0
	s_barrier
; #define PG8_STAGEB(bufoff, gbase) glds2(voffB, (gbase), voffB, (gbase) + qstep, ldsb + (bufoff))
; #define PG8_STAGEA(bufoff, rowb, v, h, kb) do { if constexpr (GATHER) glds2((v)[h][0], Ab + (kb), (v)[h][1], Ab + (kb), ldsb + (bufoff)); \
;         else glds2(voffA, Ab + (rowb) + (h) * hstep + (kb), voffA, Ab + (rowb) + (h) * hstep + qstep + (kb), ldsb + (bufoff)); } while (0)
; #define PG8_LDA(dst, b, h) do { _Pragma("unroll") for (int m = 0; m < 4; ++m) _Pragma("unroll") for (int k = 0; k < 2; ++k) dst[m][k] = *(const PG8_LAS bf16x8*)(lds + PG8_SA(b, h) + aoff + m * 2048 + k * 1024); } while (0)
; #define PG8_LDB(dst, b, h) do { _Pragma("unroll") for (int n = 0; n < 2; ++n) _Pragma("unroll") for (int k = 0; k < 2; ++k) dst[n][k] = *(const PG8_LAS bf16x8*)(lds + PG8_SB(b, h) + boff + n * 2048 + k * 1024); } while (0)
; #define PG8_WAIT_V(n) asm volatile("s_waitcnt vmcnt(" #n ")" ::: "memory")
; #define PG8_WAIT_L(n) asm volatile("s_waitcnt lgkmcnt(" #n ")" ::: "memory")
; #define PG8_BAR __builtin_amdgcn_s_barrier()
; #define PG8_SCHED __builtin_amdgcn_sched_barrier(0)
; template <class Epi, bool GATHER, int MODE, bool SPLIT = false>
; __device__ __forceinline__ void gemm_phase(PG8_LAS unsigned char* lds, const Gemm g, const Order& S, const Epi& E) {
;     ...
;         const bool has_next = S.next(ui + 1, nxt);
;         const char* nB = has_next ? (const char*)g.Bt + (size_t)nxt.e * g.bstride + (size_t)nxt.pn * tstep : cB;
;         const size_t nAr = has_next ? (size_t)nxt.pm * tstep : cAr;
;         if (has_next) { PG8_VOFF(nv, nxt); }
;         else {
; #pragma unroll
;             for (int h = 0; h < 2; ++h)
; #pragma unroll
;                 for (int i = 0; i < 2; ++i) nv[h][i] = cv[h][i]; }
;     ...
;             PG8_LDA(At, 1, 1); PG8_STAGEB(PG8_SB(1, 0), b3); PG8_STAGEB(PG8_SB(1, 1), b3 + hstep); PG8_STAGEA(PG8_SA(1, 0), cAr, cv, 0, k3);
;             PG8_WAIT_V(8); PG8_WAIT_L(0); PG8_BAR; PG8_MMA(1, 0, At, B0); PG8_MMA(1, 1, At, B1); PG8_BAR; PG8_SCHED;
;         }
;         {
;             const size_t k1 = (size_t)(nt - 1) * kstep;
;             PG8_LDB(B0, 0, 0); PG8_LDB(B1, 0, 1); PG8_SCHED; PG8_LDA(At, 0, 0); PG8_STAGEA(PG8_SA(1, 1), cAr, cv, 1, k1);
	s_add_u32 s36, s66, 0x180
	s_addc_u32 s37, s67, 0
	s_add_u32 s68, s66, 0x20180
	s_addc_u32 s69, s67, 0
	ds_read_b128 v[198:201], v181 offset:49152
	ds_read_b128 v[202:205], v181 offset:50176
	ds_read_b128 v[206:209], v181 offset:51200
	ds_read_b128 v[210:213], v181 offset:52224
	ds_read_b128 v[214:217], v181 offset:53248
	ds_read_b128 v[218:221], v181 offset:54272
	ds_read_b128 v[222:225], v181 offset:55296
	ds_read_b128 v[226:229], v181 offset:56320
	s_mov_b32 s70, m0
	s_mov_b32 m0, s56
	s_nop 0
	global_load_lds_dwordx4 v168, s[36:37]
	s_mov_b32 m0, s57
	s_nop 0
	global_load_lds_dwordx4 v168, s[68:69]
	s_mov_b32 m0, s70
	s_add_u32 s36, s66, 0x40180
	s_addc_u32 s37, s67, 0
	s_add_u32 s66, s66, 0x60180
	s_addc_u32 s67, s67, 0
	s_mov_b32 s68, m0
	s_mov_b32 m0, s60
	s_nop 0
	global_load_lds_dwordx4 v168, s[36:37]
	s_mov_b32 m0, s61
	s_nop 0
	global_load_lds_dwordx4 v168, s[66:67]
	s_mov_b32 m0, s68
	s_add_u32 s36, s27, 0x180
	s_addc_u32 s37, s29, 0
	s_mov_b32 s27, m0
	s_mov_b32 m0, s58
	s_nop 0
	global_load_lds_dwordx4 v191, s[36:37]
	s_mov_b32 m0, s59
	s_nop 0
	global_load_lds_dwordx4 v192, s[36:37]
	s_mov_b32 m0, s27
	s_waitcnt vmcnt(8)
	s_waitcnt lgkmcnt(0)
	s_setprio 1
	s_barrier
	s_waitcnt lgkmcnt(7)
	v_mfma_i32_16x16x64_i8 v[62:65], v[130:133], v[198:201], v[62:65]
	v_mfma_i32_16x16x64_i8 v[58:61], v[140:143], v[198:201], v[58:61]
	s_waitcnt lgkmcnt(5)
	v_mfma_i32_16x16x64_i8 v[46:49], v[130:133], v[206:209], v[46:49]
	v_mfma_i32_16x16x64_i8 v[42:45], v[140:143], v[206:209], v[42:45]
	s_waitcnt lgkmcnt(3)
	v_mfma_i32_16x16x64_i8 v[38:41], v[130:133], v[214:217], v[38:41]
	v_mfma_i32_16x16x64_i8 v[34:37], v[140:143], v[214:217], v[34:37]
	s_waitcnt lgkmcnt(1)
	v_mfma_i32_16x16x64_i8 v[22:25], v[130:133], v[222:225], v[22:25]
	v_mfma_i32_16x16x64_i8 v[18:21], v[140:143], v[222:225], v[18:21]
	v_mfma_i32_16x16x64_i8 v[62:65], v[134:137], v[202:205], v[62:65]
	v_mfma_i32_16x16x64_i8 v[58:61], v[144:147], v[202:205], v[58:61]
	v_mfma_i32_16x16x64_i8 v[46:49], v[134:137], v[210:213], v[46:49]
	v_mfma_i32_16x16x64_i8 v[42:45], v[144:147], v[210:213], v[42:45]
	v_mfma_i32_16x16x64_i8 v[38:41], v[134:137], v[218:221], v[38:41]
	v_mfma_i32_16x16x64_i8 v[34:37], v[144:147], v[218:221], v[34:37]
	s_waitcnt lgkmcnt(0)
	v_mfma_i32_16x16x64_i8 v[22:25], v[134:137], v[226:229], v[22:25]
	v_mfma_i32_16x16x64_i8 v[18:21], v[144:147], v[226:229], v[18:21]
	s_setprio 0
	s_setprio 1
	v_mfma_i32_16x16x64_i8 v[54:57], v[148:151], v[198:201], v[54:57]
	v_mfma_i32_16x16x64_i8 v[50:53], v[156:159], v[198:201], v[50:53]
	v_mfma_i32_16x16x64_i8 v[30:33], v[148:151], v[206:209], v[30:33]
	v_mfma_i32_16x16x64_i8 v[26:29], v[156:159], v[206:209], v[26:29]
	v_mfma_i32_16x16x64_i8 v[14:17], v[148:151], v[214:217], v[14:17]
	v_mfma_i32_16x16x64_i8 v[10:13], v[156:159], v[214:217], v[10:13]
	v_mfma_i32_16x16x64_i8 v[6:9], v[148:151], v[222:225], v[6:9]
	v_mfma_i32_16x16x64_i8 v[2:5], v[156:159], v[222:225], v[2:5]
	s_nop 0
	v_mfma_i32_16x16x64_i8 v[54:57], v[152:155], v[202:205], v[54:57]
	v_mfma_i32_16x16x64_i8 v[50:53], v[194:197], v[202:205], v[50:53]
	v_mfma_i32_16x16x64_i8 v[30:33], v[152:155], v[210:213], v[30:33]
	v_mfma_i32_16x16x64_i8 v[26:29], v[194:197], v[210:213], v[26:29]
	v_mfma_i32_16x16x64_i8 v[14:17], v[152:155], v[218:221], v[14:17]
	v_mfma_i32_16x16x64_i8 v[10:13], v[194:197], v[218:221], v[10:13]
	v_mfma_i32_16x16x64_i8 v[6:9], v[152:155], v[226:229], v[6:9]
	v_mfma_i32_16x16x64_i8 v[2:5], v[194:197], v[226:229], v[2:5]
	s_setprio 0
	s_barrier
	s_add_i32 s11, s11, 2
	s_add_u32 s30, s30, 0x100
	s_addc_u32 s31, s31, 0
	s_cmp_lt_u32 s11, 12
	s_cbranch_scc1 .LBB0_802
	v_readfirstlane_b32 s28, v230
	s_and_b64 s[98:99], s[4:5], exec
	s_cbranch_scc0 .Lp8_nonext
	v_lshl_add_u32 v184, v231, 11, v167
	v_lshl_add_u32 v185, v232, 11, v167
	v_lshl_add_u32 v186, v233, 11, v167
	v_lshl_add_u32 v187, v234, 11, v167
.Lp8_nonext:
	ds_read_b128 v[140:143], v179
	ds_read_b128 v[144:147], v179 offset:1024
	ds_read_b128 v[148:151], v179 offset:2048
	ds_read_b128 v[152:155], v179 offset:3072
	ds_read_b128 v[156:159], v180
	ds_read_b128 v[130:133], v180 offset:1024
	ds_read_b128 v[192:195], v180 offset:2048
	ds_read_b128 v[134:137], v180 offset:3072
	s_ashr_i32 s29, s28, 31
	s_lshl_b64 s[30:31], s[28:29], 23
	s_add_u32 s11, s41, s30
	s_addc_u32 s29, s42, s31
	s_ashr_i32 s27, s26, 31
	s_lshl_b64 s[30:31], s[26:27], 19
	s_add_u32 s30, s11, s30
	s_addc_u32 s31, s29, s31
	s_and_b64 s[4:5], s[4:5], exec
	s_cselect_b32 s5, s31, s35
	s_cselect_b32 s4, s30, s34
	ds_read_b128 v[196:199], v181
	ds_read_b128 v[200:203], v181 offset:1024
	ds_read_b128 v[204:207], v181 offset:2048
	ds_read_b128 v[208:211], v181 offset:3072
	ds_read_b128 v[212:215], v181 offset:4096
	ds_read_b128 v[216:219], v181 offset:5120
	ds_read_b128 v[220:223], v181 offset:6144
	ds_read_b128 v[224:227], v181 offset:7168
	s_mov_b32 s11, m0
	s_mov_b32 m0, s62
	s_nop 0
	global_load_lds_dwordx4 v189, s[20:21]
	s_mov_b32 m0, s63
	s_nop 0
	global_load_lds_dwordx4 v190, s[20:21]
	s_mov_b32 m0, s11
	s_waitcnt vmcnt(8)
	s_waitcnt lgkmcnt(0)
	s_setprio 1
	s_barrier
; #define PG8_STAGEB(bufoff, gbase) glds2(voffB, (gbase), voffB, (gbase) + qstep, ldsb + (bufoff))
; #define PG8_STAGEA(bufoff, rowb, v, h, kb) do { if constexpr (GATHER) glds2((v)[h][0], Ab + (kb), (v)[h][1], Ab + (kb), ldsb + (bufoff)); \
;         else glds2(voffA, Ab + (rowb) + (h) * hstep + (kb), voffA, Ab + (rowb) + (h) * hstep + qstep + (kb), ldsb + (bufoff)); } while (0)
; #define PG8_LDA(dst, b, h) do { _Pragma("unroll") for (int m = 0; m < 4; ++m) _Pragma("unroll") for (int k = 0; k < 2; ++k) dst[m][k] = *(const PG8_LAS bf16x8*)(lds + PG8_SA(b, h) + aoff + m * 2048 + k * 1024); } while (0)
; #define PG8_LDB(dst, b, h) do { _Pragma("unroll") for (int n = 0; n < 2; ++n) _Pragma("unroll") for (int k = 0; k < 2; ++k) dst[n][k] = *(const PG8_LAS bf16x8*)(lds + PG8_SB(b, h) + boff + n * 2048 + k * 1024); } while (0)
; #define PG8_WAIT_V(n) asm volatile("s_waitcnt vmcnt(" #n ")" ::: "memory")
; #define PG8_WAIT_L(n) asm volatile("s_waitcnt lgkmcnt(" #n ")" ::: "memory")
; #define PG8_BAR __builtin_amdgcn_s_barrier()
; #define PG8_SCHED __builtin_amdgcn_sched_barrier(0)
; template <class Epi, bool GATHER, int MODE, bool SPLIT = false>
; __device__ __forceinline__ void gemm_phase(PG8_LAS unsigned char* lds, const Gemm g, const Order& S, const Epi& E) {
;     ...
;             PG8_LDB(B0, 0, 0); PG8_LDB(B1, 0, 1); PG8_SCHED; PG8_LDA(At, 0, 0); PG8_STAGEA(PG8_SA(1, 1), cAr, cv, 1, k1);
;             PG8_WAIT_V(8); PG8_WAIT_L(0); PG8_BAR; PG8_MMA(0, 0, At, B0); PG8_MMA(0, 1, At, B1); PG8_BAR; PG8_SCHED;
;             PG8_LDA(At, 0, 1); PG8_STAGEB(PG8_SB(0, 0), nB); PG8_STAGEB(PG8_SB(0, 1), nB + hstep); PG8_STAGEA(PG8_SA(0, 0), nAr, nv, 0, 0);
;             PG8_WAIT_V(8); PG8_WAIT_L(0); PG8_BAR; PG8_MMA(1, 0, At, B0); PG8_MMA(1, 1, At, B1); PG8_BAR; PG8_SCHED;
	s_waitcnt lgkmcnt(7)
	v_mfma_i32_16x16x64_i8 v[126:129], v[140:143], v[196:199], v[126:129]
	v_mfma_i32_16x16x64_i8 v[122:125], v[148:151], v[196:199], v[122:125]
	s_waitcnt lgkmcnt(5)
	v_mfma_i32_16x16x64_i8 v[118:121], v[140:143], v[204:207], v[118:121]
	v_mfma_i32_16x16x64_i8 v[106:109], v[148:151], v[204:207], v[106:109]
	s_waitcnt lgkmcnt(3)
	v_mfma_i32_16x16x64_i8 v[102:105], v[140:143], v[212:215], v[102:105]
	v_mfma_i32_16x16x64_i8 v[90:93], v[148:151], v[212:215], v[90:93]
	s_waitcnt lgkmcnt(1)
	v_mfma_i32_16x16x64_i8 v[86:89], v[140:143], v[220:223], v[86:89]
	v_mfma_i32_16x16x64_i8 v[74:77], v[148:151], v[220:223], v[74:77]
	v_mfma_i32_16x16x64_i8 v[126:129], v[144:147], v[200:203], v[126:129]
	v_mfma_i32_16x16x64_i8 v[122:125], v[152:155], v[200:203], v[122:125]
	v_mfma_i32_16x16x64_i8 v[118:121], v[144:147], v[208:211], v[118:121]
	v_mfma_i32_16x16x64_i8 v[106:109], v[152:155], v[208:211], v[106:109]
	v_mfma_i32_16x16x64_i8 v[102:105], v[144:147], v[216:219], v[102:105]
	v_mfma_i32_16x16x64_i8 v[90:93], v[152:155], v[216:219], v[90:93]
	s_waitcnt lgkmcnt(0)
	v_mfma_i32_16x16x64_i8 v[86:89], v[144:147], v[224:227], v[86:89]
	v_mfma_i32_16x16x64_i8 v[74:77], v[152:155], v[224:227], v[74:77]
	s_setprio 0
	s_setprio 1
	v_mfma_i32_16x16x64_i8 v[114:117], v[156:159], v[196:199], v[114:117]
	v_mfma_i32_16x16x64_i8 v[110:113], v[192:195], v[196:199], v[110:113]
	v_mfma_i32_16x16x64_i8 v[98:101], v[156:159], v[204:207], v[98:101]
	v_mfma_i32_16x16x64_i8 v[94:97], v[192:195], v[204:207], v[94:97]
	v_mfma_i32_16x16x64_i8 v[82:85], v[156:159], v[212:215], v[82:85]
	v_mfma_i32_16x16x64_i8 v[78:81], v[192:195], v[212:215], v[78:81]
	v_mfma_i32_16x16x64_i8 v[70:73], v[156:159], v[220:223], v[70:73]
	v_mfma_i32_16x16x64_i8 v[66:69], v[192:195], v[220:223], v[66:69]
	s_nop 0
	v_mfma_i32_16x16x64_i8 v[114:117], v[130:133], v[200:203], v[114:117]
	v_mfma_i32_16x16x64_i8 v[110:113], v[134:137], v[200:203], v[110:113]
	v_mfma_i32_16x16x64_i8 v[98:101], v[130:133], v[208:211], v[98:101]
	v_mfma_i32_16x16x64_i8 v[94:97], v[134:137], v[208:211], v[94:97]
	v_mfma_i32_16x16x64_i8 v[82:85], v[130:133], v[216:219], v[82:85]
	v_mfma_i32_16x16x64_i8 v[78:81], v[134:137], v[216:219], v[78:81]
	v_mfma_i32_16x16x64_i8 v[70:73], v[130:133], v[224:227], v[70:73]
	v_mfma_i32_16x16x64_i8 v[66:69], v[134:137], v[224:227], v[66:69]
	s_setprio 0
	s_barrier
	s_add_u32 s34, s4, 0x20000
	ds_read_b128 v[196:199], v181 offset:16384
	ds_read_b128 v[200:203], v181 offset:17408
	ds_read_b128 v[204:207], v181 offset:18432
	ds_read_b128 v[208:211], v181 offset:19456
	ds_read_b128 v[212:215], v181 offset:20480
	ds_read_b128 v[216:219], v181 offset:21504
	ds_read_b128 v[220:223], v181 offset:22528
	ds_read_b128 v[224:227], v181 offset:23552
	s_addc_u32 s35, s5, 0
	s_mov_b32 s11, m0
	s_mov_b32 m0, s49
	s_nop 0
	global_load_lds_dwordx4 v168, s[4:5]
	s_mov_b32 m0, s50
	s_nop 0
	global_load_lds_dwordx4 v168, s[34:35]
	s_mov_b32 m0, s11
	s_add_u32 s34, s4, 0x40000
	s_addc_u32 s35, s5, 0
	s_add_u32 s36, s4, 0x60000
	s_addc_u32 s37, s5, 0
	s_mov_b32 s11, m0
	s_mov_b32 m0, s51
	s_nop 0
	global_load_lds_dwordx4 v168, s[34:35]
	s_mov_b32 m0, s52
	s_nop 0
	global_load_lds_dwordx4 v168, s[36:37]
	s_mov_b32 m0, s11
	s_nop 0
	s_mov_b32 s11, m0
	s_mov_b32 m0, s43
	s_nop 0
	global_load_lds_dwordx4 v184, s[6:7]
	s_mov_b32 m0, s53
	s_nop 0
	global_load_lds_dwordx4 v185, s[6:7]
	s_mov_b32 m0, s11
	s_waitcnt vmcnt(8)
	s_waitcnt lgkmcnt(0)
	s_setprio 1
	s_barrier
	s_waitcnt lgkmcnt(7)
	v_mfma_i32_16x16x64_i8 v[62:65], v[140:143], v[196:199], v[62:65]
	v_mfma_i32_16x16x64_i8 v[58:61], v[148:151], v[196:199], v[58:61]
	s_waitcnt lgkmcnt(5)
	v_mfma_i32_16x16x64_i8 v[46:49], v[140:143], v[204:207], v[46:49]
	v_mfma_i32_16x16x64_i8 v[42:45], v[148:151], v[204:207], v[42:45]
	s_waitcnt lgkmcnt(3)
	v_mfma_i32_16x16x64_i8 v[38:41], v[140:143], v[212:215], v[38:41]
	v_mfma_i32_16x16x64_i8 v[34:37], v[148:151], v[212:215], v[34:37]
	s_waitcnt lgkmcnt(1)
	v_mfma_i32_16x16x64_i8 v[22:25], v[140:143], v[220:223], v[22:25]
	v_mfma_i32_16x16x64_i8 v[18:21], v[148:151], v[220:223], v[18:21]
	v_mfma_i32_16x16x64_i8 v[62:65], v[144:147], v[200:203], v[62:65]
	v_mfma_i32_16x16x64_i8 v[58:61], v[152:155], v[200:203], v[58:61]
	v_mfma_i32_16x16x64_i8 v[46:49], v[144:147], v[208:211], v[46:49]
	v_mfma_i32_16x16x64_i8 v[42:45], v[152:155], v[208:211], v[42:45]
	v_mfma_i32_16x16x64_i8 v[38:41], v[144:147], v[216:219], v[38:41]
	v_mfma_i32_16x16x64_i8 v[34:37], v[152:155], v[216:219], v[34:37]
	s_waitcnt lgkmcnt(0)
	v_mfma_i32_16x16x64_i8 v[22:25], v[144:147], v[224:227], v[22:25]
	v_mfma_i32_16x16x64_i8 v[18:21], v[152:155], v[224:227], v[18:21]
	s_setprio 0
	s_setprio 1
	v_mfma_i32_16x16x64_i8 v[54:57], v[156:159], v[196:199], v[54:57]
	v_mfma_i32_16x16x64_i8 v[50:53], v[192:195], v[196:199], v[50:53]
	v_mfma_i32_16x16x64_i8 v[30:33], v[156:159], v[204:207], v[30:33]
	v_mfma_i32_16x16x64_i8 v[26:29], v[192:195], v[204:207], v[26:29]
	v_mfma_i32_16x16x64_i8 v[14:17], v[156:159], v[212:215], v[14:17]
	v_mfma_i32_16x16x64_i8 v[10:13], v[192:195], v[212:215], v[10:13]
	v_mfma_i32_16x16x64_i8 v[6:9], v[156:159], v[220:223], v[6:9]
	v_mfma_i32_16x16x64_i8 v[2:5], v[192:195], v[220:223], v[2:5]
	s_nop 0
	v_mfma_i32_16x16x64_i8 v[54:57], v[130:133], v[200:203], v[54:57]
	v_mfma_i32_16x16x64_i8 v[50:53], v[134:137], v[200:203], v[50:53]
	v_mfma_i32_16x16x64_i8 v[30:33], v[130:133], v[208:211], v[30:33]
	v_mfma_i32_16x16x64_i8 v[26:29], v[134:137], v[208:211], v[26:29]
	v_mfma_i32_16x16x64_i8 v[14:17], v[130:133], v[216:219], v[14:17]
	v_mfma_i32_16x16x64_i8 v[10:13], v[134:137], v[216:219], v[10:13]
	v_mfma_i32_16x16x64_i8 v[6:9], v[130:133], v[224:227], v[6:9]
	v_mfma_i32_16x16x64_i8 v[2:5], v[134:137], v[224:227], v[2:5]
	s_setprio 0
	s_barrier
; #define PG8_STAGEB(bufoff, gbase) glds2(voffB, (gbase), voffB, (gbase) + qstep, ldsb + (bufoff))
; #define PG8_STAGEA(bufoff, rowb, v, h, kb) do { if constexpr (GATHER) glds2((v)[h][0], Ab + (kb), (v)[h][1], Ab + (kb), ldsb + (bufoff)); \
;         else glds2(voffA, Ab + (rowb) + (h) * hstep + (kb), voffA, Ab + (rowb) + (h) * hstep + qstep + (kb), ldsb + (bufoff)); } while (0)
; #define PG8_LDA(dst, b, h) do { _Pragma("unroll") for (int m = 0; m < 4; ++m) _Pragma("unroll") for (int k = 0; k < 2; ++k) dst[m][k] = *(const PG8_LAS bf16x8*)(lds + PG8_SA(b, h) + aoff + m * 2048 + k * 1024); } while (0)
; #define PG8_LDB(dst, b, h) do { _Pragma("unroll") for (int n = 0; n < 2; ++n) _Pragma("unroll") for (int k = 0; k < 2; ++k) dst[n][k] = *(const PG8_LAS bf16x8*)(lds + PG8_SB(b, h) + boff + n * 2048 + k * 1024); } while (0)
; #define PG8_WAIT_V(n) asm volatile("s_waitcnt vmcnt(" #n ")" ::: "memory")
; #define PG8_WAIT_L(n) asm volatile("s_waitcnt lgkmcnt(" #n ")" ::: "memory")
; #define PG8_BAR __builtin_amdgcn_s_barrier()
; #define PG8_SCHED __builtin_amdgcn_sched_barrier(0)
; template <class Epi, bool GATHER, int MODE, bool SPLIT = false>
; __device__ __forceinline__ void gemm_phase(PG8_LAS unsigned char* lds, const Gemm g, const Order& S, const Epi& E) {
;     ...
;             PG8_LDB(B0, 1, 0); PG8_LDB(B1, 1, 1); PG8_SCHED; PG8_LDA(At, 1, 0); PG8_STAGEA(PG8_SA(0, 1), nAr, nv, 1, 0);
;             PG8_WAIT_V(8); PG8_WAIT_L(0); PG8_BAR; PG8_MMA(0, 0, At, B0); PG8_MMA(0, 1, At, B1); PG8_BAR; PG8_SCHED;
;             PG8_LDA(At, 1, 1); PG8_STAGEB(PG8_SB(1, 0), nB + kstep); PG8_STAGEB(PG8_SB(1, 1), nB + hstep + kstep); PG8_STAGEA(PG8_SA(1, 0), nAr, nv, 0, kstep);
;             PG8_WAIT_V(8); PG8_WAIT_L(0); PG8_BAR; PG8_MMA(1, 0, At, B0); PG8_MMA(1, 1, At, B1); PG8_BAR; PG8_SCHED;
;         }
;         if (wr == 0) PG8_BAR;
	ds_read_b128 v[130:133], v182
	ds_read_b128 v[134:137], v182 offset:1024
	ds_read_b128 v[140:143], v182 offset:2048
	ds_read_b128 v[144:147], v182 offset:3072
	ds_read_b128 v[148:151], v138
	ds_read_b128 v[152:155], v138 offset:1024
	ds_read_b128 v[156:159], v138 offset:2048
	ds_read_b128 v[190:193], v138 offset:3072
	ds_read_b128 v[194:197], v181 offset:32768
	ds_read_b128 v[198:201], v181 offset:33792
	ds_read_b128 v[202:205], v181 offset:34816
	ds_read_b128 v[206:209], v181 offset:35840
	ds_read_b128 v[210:213], v181 offset:36864
	ds_read_b128 v[214:217], v181 offset:37888
	ds_read_b128 v[218:221], v181 offset:38912
	ds_read_b128 v[222:225], v181 offset:39936
	s_mov_b32 s11, m0
	s_mov_b32 m0, s54
	s_nop 0
	global_load_lds_dwordx4 v186, s[6:7]
	s_mov_b32 m0, s55
	s_nop 0
	global_load_lds_dwordx4 v187, s[6:7]
	s_mov_b32 m0, s11
	s_waitcnt vmcnt(8)
	s_waitcnt lgkmcnt(0)
	s_setprio 1
	s_barrier
	s_waitcnt lgkmcnt(7)
	v_mfma_i32_16x16x64_i8 v[126:129], v[130:133], v[194:197], v[126:129]
	v_mfma_i32_16x16x64_i8 v[122:125], v[140:143], v[194:197], v[122:125]
	s_waitcnt lgkmcnt(5)
	v_mfma_i32_16x16x64_i8 v[118:121], v[130:133], v[202:205], v[118:121]
	v_mfma_i32_16x16x64_i8 v[106:109], v[140:143], v[202:205], v[106:109]
	s_waitcnt lgkmcnt(3)
	v_mfma_i32_16x16x64_i8 v[102:105], v[130:133], v[210:213], v[102:105]
	v_mfma_i32_16x16x64_i8 v[90:93], v[140:143], v[210:213], v[90:93]
	s_waitcnt lgkmcnt(1)
	v_mfma_i32_16x16x64_i8 v[86:89], v[130:133], v[218:221], v[86:89]
	v_mfma_i32_16x16x64_i8 v[74:77], v[140:143], v[218:221], v[74:77]
	v_mfma_i32_16x16x64_i8 v[126:129], v[134:137], v[198:201], v[126:129]
	v_mfma_i32_16x16x64_i8 v[122:125], v[144:147], v[198:201], v[122:125]
	v_mfma_i32_16x16x64_i8 v[118:121], v[134:137], v[206:209], v[118:121]
	v_mfma_i32_16x16x64_i8 v[106:109], v[144:147], v[206:209], v[106:109]
	v_mfma_i32_16x16x64_i8 v[102:105], v[134:137], v[214:217], v[102:105]
	v_mfma_i32_16x16x64_i8 v[90:93], v[144:147], v[214:217], v[90:93]
	s_waitcnt lgkmcnt(0)
	v_mfma_i32_16x16x64_i8 v[86:89], v[134:137], v[222:225], v[86:89]
	v_mfma_i32_16x16x64_i8 v[74:77], v[144:147], v[222:225], v[74:77]
	s_setprio 0
	s_setprio 1
	v_mfma_i32_16x16x64_i8 v[114:117], v[148:151], v[194:197], v[114:117]
	v_mfma_i32_16x16x64_i8 v[110:113], v[156:159], v[194:197], v[110:113]
	v_mfma_i32_16x16x64_i8 v[98:101], v[148:151], v[202:205], v[98:101]
	v_mfma_i32_16x16x64_i8 v[94:97], v[156:159], v[202:205], v[94:97]
	v_mfma_i32_16x16x64_i8 v[82:85], v[148:151], v[210:213], v[82:85]
	v_mfma_i32_16x16x64_i8 v[78:81], v[156:159], v[210:213], v[78:81]
	v_mfma_i32_16x16x64_i8 v[70:73], v[148:151], v[218:221], v[70:73]
	v_mfma_i32_16x16x64_i8 v[66:69], v[156:159], v[218:221], v[66:69]
	s_nop 0
	v_mfma_i32_16x16x64_i8 v[114:117], v[152:155], v[198:201], v[114:117]
	v_mfma_i32_16x16x64_i8 v[110:113], v[190:193], v[198:201], v[110:113]
	v_mfma_i32_16x16x64_i8 v[98:101], v[152:155], v[206:209], v[98:101]
	v_mfma_i32_16x16x64_i8 v[94:97], v[190:193], v[206:209], v[94:97]
	v_mfma_i32_16x16x64_i8 v[82:85], v[152:155], v[214:217], v[82:85]
	v_mfma_i32_16x16x64_i8 v[78:81], v[190:193], v[214:217], v[78:81]
	v_mfma_i32_16x16x64_i8 v[70:73], v[152:155], v[222:225], v[70:73]
	v_mfma_i32_16x16x64_i8 v[66:69], v[190:193], v[222:225], v[66:69]
	s_setprio 0
	s_barrier
	s_add_u32 s34, s4, 0x80
	s_addc_u32 s35, s5, 0
	s_add_u32 s36, s4, 0x20080
	ds_read_b128 v[194:197], v181 offset:49152
	ds_read_b128 v[198:201], v181 offset:50176
	ds_read_b128 v[202:205], v181 offset:51200
	ds_read_b128 v[206:209], v181 offset:52224
	ds_read_b128 v[210:213], v181 offset:53248
	ds_read_b128 v[214:217], v181 offset:54272
	ds_read_b128 v[218:221], v181 offset:55296
	ds_read_b128 v[222:225], v181 offset:56320
	s_addc_u32 s37, s5, 0
	s_mov_b32 s11, m0
	s_mov_b32 m0, s56
	s_nop 0
	global_load_lds_dwordx4 v168, s[34:35]
	s_mov_b32 m0, s57
	s_nop 0
	global_load_lds_dwordx4 v168, s[36:37]
	s_mov_b32 m0, s11
	s_add_u32 s34, s4, 0x40080
	s_addc_u32 s35, s5, 0
	s_add_u32 s4, s4, 0x60080
	s_addc_u32 s5, s5, 0
	s_mov_b32 s11, m0
	s_mov_b32 m0, s60
	s_nop 0
	global_load_lds_dwordx4 v168, s[34:35]
	s_mov_b32 m0, s61
	s_nop 0
	global_load_lds_dwordx4 v168, s[4:5]
	s_mov_b32 m0, s11
	s_mov_b32 s4, m0
	s_mov_b32 m0, s58
	s_nop 0
	global_load_lds_dwordx4 v184, s[18:19]
	s_mov_b32 m0, s59
	s_nop 0
	global_load_lds_dwordx4 v185, s[18:19]
	s_mov_b32 m0, s4
	s_waitcnt vmcnt(8)
	s_waitcnt lgkmcnt(0)
	s_setprio 1
	s_barrier
	s_waitcnt lgkmcnt(7)
	v_mfma_i32_16x16x64_i8 v[62:65], v[130:133], v[194:197], v[62:65]
	v_mfma_i32_16x16x64_i8 v[58:61], v[140:143], v[194:197], v[58:61]
	s_waitcnt lgkmcnt(5)
	v_mfma_i32_16x16x64_i8 v[46:49], v[130:133], v[202:205], v[46:49]
	v_mfma_i32_16x16x64_i8 v[42:45], v[140:143], v[202:205], v[42:45]
	s_waitcnt lgkmcnt(3)
	v_mfma_i32_16x16x64_i8 v[38:41], v[130:133], v[210:213], v[38:41]
	v_mfma_i32_16x16x64_i8 v[34:37], v[140:143], v[210:213], v[34:37]
	s_waitcnt lgkmcnt(1)
	v_mfma_i32_16x16x64_i8 v[22:25], v[130:133], v[218:221], v[22:25]
	v_mfma_i32_16x16x64_i8 v[18:21], v[140:143], v[218:221], v[18:21]
	v_mfma_i32_16x16x64_i8 v[62:65], v[134:137], v[198:201], v[62:65]
	v_mfma_i32_16x16x64_i8 v[58:61], v[144:147], v[198:201], v[58:61]
	v_mfma_i32_16x16x64_i8 v[46:49], v[134:137], v[206:209], v[46:49]
	v_mfma_i32_16x16x64_i8 v[42:45], v[144:147], v[206:209], v[42:45]
	v_mfma_i32_16x16x64_i8 v[38:41], v[134:137], v[214:217], v[38:41]
	v_mfma_i32_16x16x64_i8 v[34:37], v[144:147], v[214:217], v[34:37]
	s_waitcnt lgkmcnt(0)
	v_mfma_i32_16x16x64_i8 v[22:25], v[134:137], v[222:225], v[22:25]
	v_mfma_i32_16x16x64_i8 v[18:21], v[144:147], v[222:225], v[18:21]
	s_setprio 0
	s_setprio 1
	v_mfma_i32_16x16x64_i8 v[54:57], v[148:151], v[194:197], v[54:57]
	v_mfma_i32_16x16x64_i8 v[50:53], v[156:159], v[194:197], v[50:53]
	v_mfma_i32_16x16x64_i8 v[30:33], v[148:151], v[202:205], v[30:33]
	v_mfma_i32_16x16x64_i8 v[26:29], v[156:159], v[202:205], v[26:29]
	v_mfma_i32_16x16x64_i8 v[14:17], v[148:151], v[210:213], v[14:17]
	v_mfma_i32_16x16x64_i8 v[10:13], v[156:159], v[210:213], v[10:13]
	v_mfma_i32_16x16x64_i8 v[6:9], v[148:151], v[218:221], v[6:9]
	v_mfma_i32_16x16x64_i8 v[2:5], v[156:159], v[218:221], v[2:5]
	s_nop 0
	v_mfma_i32_16x16x64_i8 v[54:57], v[152:155], v[198:201], v[54:57]
	v_mfma_i32_16x16x64_i8 v[50:53], v[190:193], v[198:201], v[50:53]
	v_mfma_i32_16x16x64_i8 v[30:33], v[152:155], v[206:209], v[30:33]
	v_mfma_i32_16x16x64_i8 v[26:29], v[190:193], v[206:209], v[26:29]
	v_mfma_i32_16x16x64_i8 v[14:17], v[152:155], v[214:217], v[14:17]
	v_mfma_i32_16x16x64_i8 v[10:13], v[190:193], v[214:217], v[10:13]
	v_mfma_i32_16x16x64_i8 v[6:9], v[152:155], v[222:225], v[6:9]
	v_mfma_i32_16x16x64_i8 v[2:5], v[190:193], v[222:225], v[2:5]
	s_setprio 0
	s_nop 0
	s_andn2_b64 vcc, exec, s[22:23]
	s_cbranch_vccnz .LBB0_805
	s_barrier

; #define PG8_STAGEB(bufoff, gbase) glds2(voffB, (gbase), voffB, (gbase) + qstep, ldsb + (bufoff))
; #define PG8_STAGEA(bufoff, rowb, v, h, kb) do { if constexpr (GATHER) glds2((v)[h][0], Ab + (kb), (v)[h][1], Ab + (kb), ldsb + (bufoff)); \
;         else glds2(voffA, Ab + (rowb) + (h) * hstep + (kb), voffA, Ab + (rowb) + (h) * hstep + qstep + (kb), ldsb + (bufoff)); } while (0)
; #define PG8_LDA(dst, b, h) do { _Pragma("unroll") for (int m = 0; m < 4; ++m) _Pragma("unroll") for (int k = 0; k < 2; ++k) dst[m][k] = *(const PG8_LAS bf16x8*)(lds + PG8_SA(b, h) + aoff + m * 2048 + k * 1024); } while (0)
; #define PG8_LDB(dst, b, h) do { _Pragma("unroll") for (int n = 0; n < 2; ++n) _Pragma("unroll") for (int k = 0; k < 2; ++k) dst[n][k] = *(const PG8_LAS bf16x8*)(lds + PG8_SB(b, h) + boff + n * 2048 + k * 1024); } while (0)
; #define PG8_WAIT_V(n) asm volatile("s_waitcnt vmcnt(" #n ")" ::: "memory")
; #define PG8_WAIT_L(n) asm volatile("s_waitcnt lgkmcnt(" #n ")" ::: "memory")
; #define PG8_BAR __builtin_amdgcn_s_barrier()
; #define PG8_SCHED __builtin_amdgcn_sched_barrier(0)
; template <class Epi, bool GATHER, int MODE, bool SPLIT = false>
; __device__ __forceinline__ void gemm_phase(PG8_LAS unsigned char* lds, const Gemm g, const Order& S, const Epi& E) {
;     ...
;             PG8_LDB(B0, 0, 0); PG8_LDB(B1, 0, 1); PG8_SCHED; PG8_LDA(At, 0, 0); PG8_STAGEA(PG8_SA(1, 1), cAr, cv, 1, k1);
;             PG8_WAIT_V(8); PG8_WAIT_L(0); PG8_BAR; PG8_MMA(0, 0, At, B0); PG8_MMA(0, 1, At, B1); PG8_BAR; PG8_SCHED;
;             PG8_LDA(At, 0, 1); PG8_STAGEB(PG8_SB(0, 0), b2); PG8_STAGEB(PG8_SB(0, 1), b2 + hstep); PG8_STAGEA(PG8_SA(0, 0), cAr, cv, 0, k2);
;             PG8_WAIT_V(8); PG8_WAIT_L(0); PG8_BAR; PG8_MMA(1, 0, At, B0); PG8_MMA(1, 1, At, B1); PG8_BAR; PG8_SCHED;
;             PG8_LDB(B0, 1, 0); PG8_LDB(B1, 1, 1); PG8_SCHED; PG8_LDA(At, 1, 0); PG8_STAGEA(PG8_SA(0, 1), cAr, cv, 1, k2);
;             PG8_WAIT_V(8); PG8_WAIT_L(0); PG8_BAR; PG8_MMA(0, 0, At, B0); PG8_MMA(0, 1, At, B1); PG8_BAR; PG8_SCHED;
.LBB0_875:
	ds_read_b128 v[26:29], v172
	ds_read_b128 v[30:33], v172 offset:1024
	ds_read_b128 v[18:21], v172 offset:2048
	ds_read_b128 v[22:25], v172 offset:3072
	ds_read_b128 v[10:13], v173
	ds_read_b128 v[14:17], v173 offset:1024
	ds_read_b128 v[2:5], v173 offset:2048
	ds_read_b128 v[6:9], v173 offset:3072
	s_add_u32 s63, s24, s26
	s_addc_u32 s64, s25, s27
	s_add_u32 s28, s63, 0x100
	s_addc_u32 s29, s64, 0
	s_add_u32 s65, s15, s26
	ds_read_b128 v[180:183], v174
	ds_read_b128 v[184:187], v174 offset:1024
	ds_read_b128 v[188:191], v174 offset:2048
	ds_read_b128 v[192:195], v174 offset:3072
	ds_read_b128 v[196:199], v174 offset:4096
	ds_read_b128 v[200:203], v174 offset:5120
	ds_read_b128 v[204:207], v174 offset:6144
	ds_read_b128 v[208:211], v174 offset:7168
	s_addc_u32 s66, s19, s27
	s_add_u32 s70, s65, 0x80
	s_addc_u32 s71, s66, 0
	s_add_u32 s67, s58, s26
	s_addc_u32 s68, s59, s27
	s_add_u32 s80, s67, 0x80
	s_addc_u32 s81, s68, 0
	s_mov_b32 s69, m0
	s_mov_b32 m0, s53
	s_nop 0
	global_load_lds_dwordx4 v167, s[70:71]
	s_mov_b32 m0, s54
	s_nop 0
	global_load_lds_dwordx4 v167, s[80:81]
	s_mov_b32 m0, s69
	s_waitcnt vmcnt(8)
	s_waitcnt lgkmcnt(0)
	s_setprio 1
	s_barrier
	s_waitcnt lgkmcnt(6)
	v_mfma_f32_16x16x128_f8f6f4 v[158:161], v[26:33], v[180:187], v[158:161]
	v_mfma_f32_16x16x128_f8f6f4 v[154:157], v[18:25], v[180:187], v[154:157]
	s_waitcnt lgkmcnt(4)
	v_mfma_f32_16x16x128_f8f6f4 v[150:153], v[26:33], v[188:195], v[150:153]
	v_mfma_f32_16x16x128_f8f6f4 v[146:149], v[18:25], v[188:195], v[146:149]
	s_waitcnt lgkmcnt(2)
	v_mfma_f32_16x16x128_f8f6f4 v[142:145], v[26:33], v[196:203], v[142:145]
	v_mfma_f32_16x16x128_f8f6f4 v[138:141], v[18:25], v[196:203], v[138:141]
	s_waitcnt lgkmcnt(0)
	v_mfma_f32_16x16x128_f8f6f4 v[134:137], v[26:33], v[204:211], v[134:137]
	v_mfma_f32_16x16x128_f8f6f4 v[130:133], v[18:25], v[204:211], v[130:133]
	s_setprio 0
	s_setprio 1
	v_mfma_f32_16x16x128_f8f6f4 v[126:129], v[10:17], v[180:187], v[126:129]
	v_mfma_f32_16x16x128_f8f6f4 v[122:125], v[2:9], v[180:187], v[122:125]
	v_mfma_f32_16x16x128_f8f6f4 v[118:121], v[10:17], v[188:195], v[118:121]
	v_mfma_f32_16x16x128_f8f6f4 v[114:117], v[2:9], v[188:195], v[114:117]
	v_mfma_f32_16x16x128_f8f6f4 v[110:113], v[10:17], v[196:203], v[110:113]
	v_mfma_f32_16x16x128_f8f6f4 v[106:109], v[2:9], v[196:203], v[106:109]
	v_mfma_f32_16x16x128_f8f6f4 v[102:105], v[10:17], v[204:211], v[102:105]
	v_mfma_f32_16x16x128_f8f6f4 v[98:101], v[2:9], v[204:211], v[98:101]
	s_setprio 0
	s_barrier
	s_add_u32 s70, s63, 0x20100
	s_addc_u32 s71, s64, 0
	ds_read_b128 v[180:183], v174 offset:16384
	ds_read_b128 v[184:187], v174 offset:17408
	ds_read_b128 v[188:191], v174 offset:18432
	ds_read_b128 v[192:195], v174 offset:19456
	ds_read_b128 v[196:199], v174 offset:20480
	ds_read_b128 v[200:203], v174 offset:21504
	ds_read_b128 v[204:207], v174 offset:22528
	ds_read_b128 v[208:211], v174 offset:23552
	s_mov_b32 s69, m0
	s_mov_b32 m0, s21
	s_nop 0
	global_load_lds_dwordx4 v166, s[28:29]
	s_mov_b32 m0, s41
	s_nop 0
	global_load_lds_dwordx4 v166, s[70:71]
	s_mov_b32 m0, s69
	s_add_u32 s28, s63, 0x40100
	s_addc_u32 s29, s64, 0
	s_add_u32 s70, s63, 0x60100
	s_addc_u32 s71, s64, 0
	s_mov_b32 s69, m0
	s_mov_b32 m0, s42
	s_nop 0
	global_load_lds_dwordx4 v166, s[28:29]
	s_mov_b32 m0, s43
	s_nop 0
	global_load_lds_dwordx4 v166, s[70:71]
	s_mov_b32 m0, s69
	s_add_u32 s28, s1, s26
	s_addc_u32 s29, s57, s27
	s_add_u32 s80, s28, 0x100
	s_addc_u32 s81, s29, 0
	s_add_u32 s69, s60, s26
	s_addc_u32 s70, s61, s27
	s_add_u32 s82, s69, 0x100
	s_addc_u32 s83, s70, 0
	s_mov_b32 s71, m0
	s_mov_b32 m0, s37
	s_nop 0
	global_load_lds_dwordx4 v167, s[80:81]
	s_mov_b32 m0, s44
	s_nop 0
	global_load_lds_dwordx4 v167, s[82:83]
	s_mov_b32 m0, s71
	s_waitcnt vmcnt(8)
	s_waitcnt lgkmcnt(0)
	s_setprio 1
	s_barrier
	s_waitcnt lgkmcnt(6)
	v_mfma_f32_16x16x128_f8f6f4 v[94:97], v[26:33], v[180:187], v[94:97]
	v_mfma_f32_16x16x128_f8f6f4 v[90:93], v[18:25], v[180:187], v[90:93]
	s_waitcnt lgkmcnt(4)
	v_mfma_f32_16x16x128_f8f6f4 v[86:89], v[26:33], v[188:195], v[86:89]
	v_mfma_f32_16x16x128_f8f6f4 v[82:85], v[18:25], v[188:195], v[82:85]
	s_waitcnt lgkmcnt(2)
	v_mfma_f32_16x16x128_f8f6f4 v[78:81], v[26:33], v[196:203], v[78:81]
	v_mfma_f32_16x16x128_f8f6f4 v[74:77], v[18:25], v[196:203], v[74:77]
	s_waitcnt lgkmcnt(0)
	v_mfma_f32_16x16x128_f8f6f4 v[70:73], v[26:33], v[204:211], v[70:73]
	v_mfma_f32_16x16x128_f8f6f4 v[66:69], v[18:25], v[204:211], v[66:69]
	s_setprio 0
	s_setprio 1
	v_mfma_f32_16x16x128_f8f6f4 v[62:65], v[10:17], v[180:187], v[62:65]
	v_mfma_f32_16x16x128_f8f6f4 v[58:61], v[2:9], v[180:187], v[58:61]
	v_mfma_f32_16x16x128_f8f6f4 v[54:57], v[10:17], v[188:195], v[54:57]
	v_mfma_f32_16x16x128_f8f6f4 v[50:53], v[2:9], v[188:195], v[50:53]
	v_mfma_f32_16x16x128_f8f6f4 v[46:49], v[10:17], v[196:203], v[46:49]
	v_mfma_f32_16x16x128_f8f6f4 v[42:45], v[2:9], v[196:203], v[42:45]
	v_mfma_f32_16x16x128_f8f6f4 v[38:41], v[10:17], v[204:211], v[38:41]
	v_mfma_f32_16x16x128_f8f6f4 v[34:37], v[2:9], v[204:211], v[34:37]
	s_setprio 0
	s_barrier
	ds_read_b128 v[18:21], v175
	ds_read_b128 v[22:25], v175 offset:1024
	ds_read_b128 v[26:29], v175 offset:2048
	ds_read_b128 v[30:33], v175 offset:3072
	ds_read_b128 v[10:13], v176
	ds_read_b128 v[14:17], v176 offset:1024
	ds_read_b128 v[2:5], v176 offset:2048
	ds_read_b128 v[6:9], v176 offset:3072
	ds_read_b128 v[180:183], v174 offset:32768
	ds_read_b128 v[184:187], v174 offset:33792
	ds_read_b128 v[188:191], v174 offset:34816
	ds_read_b128 v[192:195], v174 offset:35840
	ds_read_b128 v[196:199], v174 offset:36864
	ds_read_b128 v[200:203], v174 offset:37888
	ds_read_b128 v[204:207], v174 offset:38912
	ds_read_b128 v[208:211], v174 offset:39936
	s_add_u32 s80, s65, 0x100
	s_addc_u32 s81, s66, 0
	s_add_u32 s66, s67, 0x100
	s_addc_u32 s67, s68, 0
	s_mov_b32 s65, m0
	s_mov_b32 m0, s45
	s_nop 0
	global_load_lds_dwordx4 v167, s[80:81]
	s_mov_b32 m0, s46
	s_nop 0
	global_load_lds_dwordx4 v167, s[66:67]
	s_mov_b32 m0, s65
	s_waitcnt vmcnt(8)
	s_waitcnt lgkmcnt(0)
	s_setprio 1
	s_barrier
; #define PG8_STAGEB(bufoff, gbase) glds2(voffB, (gbase), voffB, (gbase) + qstep, ldsb + (bufoff))
; #define PG8_STAGEA(bufoff, rowb, v, h, kb) do { if constexpr (GATHER) glds2((v)[h][0], Ab + (kb), (v)[h][1], Ab + (kb), ldsb + (bufoff)); \
;         else glds2(voffA, Ab + (rowb) + (h) * hstep + (kb), voffA, Ab + (rowb) + (h) * hstep + qstep + (kb), ldsb + (bufoff)); } while (0)
; #define PG8_LDA(dst, b, h) do { _Pragma("unroll") for (int m = 0; m < 4; ++m) _Pragma("unroll") for (int k = 0; k < 2; ++k) dst[m][k] = *(const PG8_LAS bf16x8*)(lds + PG8_SA(b, h) + aoff + m * 2048 + k * 1024); } while (0)
; #define PG8_LDB(dst, b, h) do { _Pragma("unroll") for (int n = 0; n < 2; ++n) _Pragma("unroll") for (int k = 0; k < 2; ++k) dst[n][k] = *(const PG8_LAS bf16x8*)(lds + PG8_SB(b, h) + boff + n * 2048 + k * 1024); } while (0)
; #define PG8_WAIT_V(n) asm volatile("s_waitcnt vmcnt(" #n ")" ::: "memory")
; #define PG8_WAIT_L(n) asm volatile("s_waitcnt lgkmcnt(" #n ")" ::: "memory")
; #define PG8_BAR __builtin_amdgcn_s_barrier()
; #define PG8_SCHED __builtin_amdgcn_sched_barrier(0)
; template <class Epi, bool GATHER, int MODE, bool SPLIT = false>
; __device__ __forceinline__ void gemm_phase(PG8_LAS unsigned char* lds, const Gemm g, const Order& S, const Epi& E) {
;     ...
;             PG8_LDA(At, 1, 1); PG8_STAGEB(PG8_SB(1, 0), b3); PG8_STAGEB(PG8_SB(1, 1), b3 + hstep); PG8_STAGEA(PG8_SA(1, 0), cAr, cv, 0, k3);
;             PG8_WAIT_V(8); PG8_WAIT_L(0); PG8_BAR; PG8_MMA(1, 0, At, B0); PG8_MMA(1, 1, At, B1); PG8_BAR; PG8_SCHED;
;         }
;         {
;             const size_t k1 = (size_t)(nt - 1) * kstep;
;             PG8_LDB(B0, 0, 0); PG8_LDB(B1, 0, 1); PG8_SCHED; PG8_LDA(At, 0, 0); PG8_STAGEA(PG8_SA(1, 1), cAr, cv, 1, k1);
	s_waitcnt lgkmcnt(6)
	v_mfma_f32_16x16x128_f8f6f4 v[158:161], v[18:25], v[180:187], v[158:161]
	v_mfma_f32_16x16x128_f8f6f4 v[154:157], v[26:33], v[180:187], v[154:157]
	s_waitcnt lgkmcnt(4)
	v_mfma_f32_16x16x128_f8f6f4 v[150:153], v[18:25], v[188:195], v[150:153]
	v_mfma_f32_16x16x128_f8f6f4 v[146:149], v[26:33], v[188:195], v[146:149]
	s_waitcnt lgkmcnt(2)
	v_mfma_f32_16x16x128_f8f6f4 v[142:145], v[18:25], v[196:203], v[142:145]
	v_mfma_f32_16x16x128_f8f6f4 v[138:141], v[26:33], v[196:203], v[138:141]
	s_waitcnt lgkmcnt(0)
	v_mfma_f32_16x16x128_f8f6f4 v[134:137], v[18:25], v[204:211], v[134:137]
	v_mfma_f32_16x16x128_f8f6f4 v[130:133], v[26:33], v[204:211], v[130:133]
	s_setprio 0
	s_setprio 1
	v_mfma_f32_16x16x128_f8f6f4 v[126:129], v[10:17], v[180:187], v[126:129]
	v_mfma_f32_16x16x128_f8f6f4 v[122:125], v[2:9], v[180:187], v[122:125]
	v_mfma_f32_16x16x128_f8f6f4 v[118:121], v[10:17], v[188:195], v[118:121]
	v_mfma_f32_16x16x128_f8f6f4 v[114:117], v[2:9], v[188:195], v[114:117]
	v_mfma_f32_16x16x128_f8f6f4 v[110:113], v[10:17], v[196:203], v[110:113]
	v_mfma_f32_16x16x128_f8f6f4 v[106:109], v[2:9], v[196:203], v[106:109]
	v_mfma_f32_16x16x128_f8f6f4 v[102:105], v[10:17], v[204:211], v[102:105]
	v_mfma_f32_16x16x128_f8f6f4 v[98:101], v[2:9], v[204:211], v[98:101]
	s_setprio 0
	s_barrier
	s_add_u32 s66, s63, 0x180
	s_addc_u32 s67, s64, 0
	s_add_u32 s80, s63, 0x20180
	s_addc_u32 s81, s64, 0
	ds_read_b128 v[180:183], v174 offset:49152
	ds_read_b128 v[184:187], v174 offset:50176
	ds_read_b128 v[188:191], v174 offset:51200
	ds_read_b128 v[192:195], v174 offset:52224
	ds_read_b128 v[196:199], v174 offset:53248
	ds_read_b128 v[200:203], v174 offset:54272
	ds_read_b128 v[204:207], v174 offset:55296
	ds_read_b128 v[208:211], v174 offset:56320
	s_mov_b32 s65, m0
	s_mov_b32 m0, s47
	s_nop 0
	global_load_lds_dwordx4 v166, s[66:67]
	s_mov_b32 m0, s48
	s_nop 0
	global_load_lds_dwordx4 v166, s[80:81]
	s_mov_b32 m0, s65
	s_add_u32 s66, s63, 0x40180
	s_addc_u32 s67, s64, 0
	s_add_u32 s80, s63, 0x60180
	s_addc_u32 s81, s64, 0
	s_add_u32 s28, s28, 0x180
	s_addc_u32 s29, s29, 0
	s_mov_b32 s63, m0
	s_mov_b32 m0, s51
	s_nop 0
	global_load_lds_dwordx4 v166, s[66:67]
	s_mov_b32 m0, s52
	s_nop 0
	global_load_lds_dwordx4 v166, s[80:81]
	s_mov_b32 m0, s63
	s_add_u32 s64, s69, 0x180
	s_addc_u32 s65, s70, 0
	s_mov_b32 s63, m0
	s_mov_b32 m0, s49
	s_nop 0
	global_load_lds_dwordx4 v167, s[28:29]
	s_mov_b32 m0, s50
	s_nop 0
	global_load_lds_dwordx4 v167, s[64:65]
	s_mov_b32 m0, s63
	s_waitcnt vmcnt(8)
	s_waitcnt lgkmcnt(0)
	s_setprio 1
	s_barrier
	s_waitcnt lgkmcnt(6)
	v_mfma_f32_16x16x128_f8f6f4 v[94:97], v[18:25], v[180:187], v[94:97]
	v_mfma_f32_16x16x128_f8f6f4 v[90:93], v[26:33], v[180:187], v[90:93]
	s_waitcnt lgkmcnt(4)
	v_mfma_f32_16x16x128_f8f6f4 v[86:89], v[18:25], v[188:195], v[86:89]
	v_mfma_f32_16x16x128_f8f6f4 v[82:85], v[26:33], v[188:195], v[82:85]
	s_waitcnt lgkmcnt(2)
	v_mfma_f32_16x16x128_f8f6f4 v[78:81], v[18:25], v[196:203], v[78:81]
	v_mfma_f32_16x16x128_f8f6f4 v[74:77], v[26:33], v[196:203], v[74:77]
	s_waitcnt lgkmcnt(0)
	v_mfma_f32_16x16x128_f8f6f4 v[70:73], v[18:25], v[204:211], v[70:73]
	v_mfma_f32_16x16x128_f8f6f4 v[66:69], v[26:33], v[204:211], v[66:69]
	s_setprio 0
	s_setprio 1
	v_mfma_f32_16x16x128_f8f6f4 v[62:65], v[10:17], v[180:187], v[62:65]
	v_mfma_f32_16x16x128_f8f6f4 v[58:61], v[2:9], v[180:187], v[58:61]
	v_mfma_f32_16x16x128_f8f6f4 v[54:57], v[10:17], v[188:195], v[54:57]
	v_mfma_f32_16x16x128_f8f6f4 v[50:53], v[2:9], v[188:195], v[50:53]
	v_mfma_f32_16x16x128_f8f6f4 v[46:49], v[10:17], v[196:203], v[46:49]
	v_mfma_f32_16x16x128_f8f6f4 v[42:45], v[2:9], v[196:203], v[42:45]
	v_mfma_f32_16x16x128_f8f6f4 v[38:41], v[10:17], v[204:211], v[38:41]
	v_mfma_f32_16x16x128_f8f6f4 v[34:37], v[2:9], v[204:211], v[34:37]
	s_setprio 0
	s_barrier
	s_add_i32 s62, s62, 2
	s_add_u32 s26, s26, 0x100
	s_addc_u32 s27, s27, 0
	s_cmp_lt_u32 s62, 12
	s_cbranch_scc1 .LBB0_875
	v_readfirstlane_b32 s18, v230
	ds_read_b128 v[26:29], v172
	ds_read_b128 v[30:33], v172 offset:1024
	ds_read_b128 v[18:21], v172 offset:2048
	ds_read_b128 v[22:25], v172 offset:3072
	ds_read_b128 v[10:13], v173
	ds_read_b128 v[14:17], v173 offset:1024
	ds_read_b128 v[2:5], v173 offset:2048
	ds_read_b128 v[6:9], v173 offset:3072
	s_ashr_i32 s19, s18, 31
	s_lshl_b64 s[26:27], s[18:19], 22
	s_add_u32 s19, s35, s26
	s_addc_u32 s28, s36, s27
	s_ashr_i32 s15, s14, 31
	s_lshl_b64 s[26:27], s[14:15], 19
	s_add_u32 s26, s19, s26
	s_addc_u32 s27, s28, s27
	s_lshl_b64 s[28:29], s[16:17], 19
	s_and_b64 s[58:59], exec, s[2:3]
	s_cselect_b32 s25, s27, s25
	s_cselect_b32 s24, s26, s24
	s_cselect_b32 s15, s29, s23
	s_cselect_b32 s17, s28, s22
	ds_read_b128 v[180:183], v174
	ds_read_b128 v[184:187], v174 offset:1024
	ds_read_b128 v[188:191], v174 offset:2048
	ds_read_b128 v[192:195], v174 offset:3072
	ds_read_b128 v[196:199], v174 offset:4096
	ds_read_b128 v[200:203], v174 offset:5120
	ds_read_b128 v[204:207], v174 offset:6144
	ds_read_b128 v[208:211], v174 offset:7168
	s_add_u32 s22, s1, 0x40780
	s_addc_u32 s23, s57, 0
	s_add_u32 s58, s1, 0x60780
	s_addc_u32 s59, s57, 0
	s_mov_b32 s1, m0
	s_mov_b32 m0, s53
	s_nop 0
	global_load_lds_dwordx4 v167, s[22:23]
	s_mov_b32 m0, s54
	s_nop 0
	global_load_lds_dwordx4 v167, s[58:59]
	s_mov_b32 m0, s1
	s_waitcnt vmcnt(8)
	s_waitcnt lgkmcnt(0)
	s_setprio 1
	s_barrier
; #define PG8_STAGEB(bufoff, gbase) glds2(voffB, (gbase), voffB, (gbase) + qstep, ldsb + (bufoff))
; #define PG8_STAGEA(bufoff, rowb, v, h, kb) do { if constexpr (GATHER) glds2((v)[h][0], Ab + (kb), (v)[h][1], Ab + (kb), ldsb + (bufoff)); \
;         else glds2(voffA, Ab + (rowb) + (h) * hstep + (kb), voffA, Ab + (rowb) + (h) * hstep + qstep + (kb), ldsb + (bufoff)); } while (0)
; #define PG8_LDA(dst, b, h) do { _Pragma("unroll") for (int m = 0; m < 4; ++m) _Pragma("unroll") for (int k = 0; k < 2; ++k) dst[m][k] = *(const PG8_LAS bf16x8*)(lds + PG8_SA(b, h) + aoff + m * 2048 + k * 1024); } while (0)
; #define PG8_LDB(dst, b, h) do { _Pragma("unroll") for (int n = 0; n < 2; ++n) _Pragma("unroll") for (int k = 0; k < 2; ++k) dst[n][k] = *(const PG8_LAS bf16x8*)(lds + PG8_SB(b, h) + boff + n * 2048 + k * 1024); } while (0)
; #define PG8_WAIT_V(n) asm volatile("s_waitcnt vmcnt(" #n ")" ::: "memory")
; #define PG8_WAIT_L(n) asm volatile("s_waitcnt lgkmcnt(" #n ")" ::: "memory")
; #define PG8_BAR __builtin_amdgcn_s_barrier()
; #define PG8_SCHED __builtin_amdgcn_sched_barrier(0)
; template <class Epi, bool GATHER, int MODE, bool SPLIT = false>
; __device__ __forceinline__ void gemm_phase(PG8_LAS unsigned char* lds, const Gemm g, const Order& S, const Epi& E) {
;     ...
;             PG8_LDB(B0, 0, 0); PG8_LDB(B1, 0, 1); PG8_SCHED; PG8_LDA(At, 0, 0); PG8_STAGEA(PG8_SA(1, 1), cAr, cv, 1, k1);
;             PG8_WAIT_V(8); PG8_WAIT_L(0); PG8_BAR; PG8_MMA(0, 0, At, B0); PG8_MMA(0, 1, At, B1); PG8_BAR; PG8_SCHED;
;             PG8_LDA(At, 0, 1); PG8_STAGEB(PG8_SB(0, 0), nB); PG8_STAGEB(PG8_SB(0, 1), nB + hstep); PG8_STAGEA(PG8_SA(0, 0), nAr, nv, 0, 0);
;             PG8_WAIT_V(8); PG8_WAIT_L(0); PG8_BAR; PG8_MMA(1, 0, At, B0); PG8_MMA(1, 1, At, B1); PG8_BAR; PG8_SCHED;
;             PG8_LDB(B0, 1, 0); PG8_LDB(B1, 1, 1); PG8_SCHED; PG8_LDA(At, 1, 0); PG8_STAGEA(PG8_SA(0, 1), nAr, nv, 1, 0);
;             PG8_WAIT_V(8); PG8_WAIT_L(0); PG8_BAR; PG8_MMA(0, 0, At, B0); PG8_MMA(0, 1, At, B1); PG8_BAR; PG8_SCHED;
	s_waitcnt lgkmcnt(6)
	v_mfma_f32_16x16x128_f8f6f4 v[158:161], v[26:33], v[180:187], v[158:161]
	v_mfma_f32_16x16x128_f8f6f4 v[154:157], v[18:25], v[180:187], v[154:157]
	s_waitcnt lgkmcnt(4)
	v_mfma_f32_16x16x128_f8f6f4 v[150:153], v[26:33], v[188:195], v[150:153]
	v_mfma_f32_16x16x128_f8f6f4 v[146:149], v[18:25], v[188:195], v[146:149]
	s_waitcnt lgkmcnt(2)
	v_mfma_f32_16x16x128_f8f6f4 v[142:145], v[26:33], v[196:203], v[142:145]
	v_mfma_f32_16x16x128_f8f6f4 v[138:141], v[18:25], v[196:203], v[138:141]
	s_waitcnt lgkmcnt(0)
	v_mfma_f32_16x16x128_f8f6f4 v[134:137], v[26:33], v[204:211], v[134:137]
	v_mfma_f32_16x16x128_f8f6f4 v[130:133], v[18:25], v[204:211], v[130:133]
	s_setprio 0
	s_setprio 1
	v_mfma_f32_16x16x128_f8f6f4 v[126:129], v[10:17], v[180:187], v[126:129]
	v_mfma_f32_16x16x128_f8f6f4 v[122:125], v[2:9], v[180:187], v[122:125]
	v_mfma_f32_16x16x128_f8f6f4 v[118:121], v[10:17], v[188:195], v[118:121]
	v_mfma_f32_16x16x128_f8f6f4 v[114:117], v[2:9], v[188:195], v[114:117]
	v_mfma_f32_16x16x128_f8f6f4 v[110:113], v[10:17], v[196:203], v[110:113]
	v_mfma_f32_16x16x128_f8f6f4 v[106:109], v[2:9], v[196:203], v[106:109]
	v_mfma_f32_16x16x128_f8f6f4 v[102:105], v[10:17], v[204:211], v[102:105]
	v_mfma_f32_16x16x128_f8f6f4 v[98:101], v[2:9], v[204:211], v[98:101]
	s_setprio 0
	s_barrier
	s_add_u32 s22, s24, 0x20000
	s_addc_u32 s23, s25, 0
	ds_read_b128 v[180:183], v174 offset:16384
	ds_read_b128 v[184:187], v174 offset:17408
	ds_read_b128 v[188:191], v174 offset:18432
	ds_read_b128 v[192:195], v174 offset:19456
	ds_read_b128 v[196:199], v174 offset:20480
	ds_read_b128 v[200:203], v174 offset:21504
	ds_read_b128 v[204:207], v174 offset:22528
	ds_read_b128 v[208:211], v174 offset:23552
	s_mov_b32 s1, m0
	s_mov_b32 m0, s21
	s_nop 0
	global_load_lds_dwordx4 v166, s[24:25]
	s_mov_b32 m0, s41
	s_nop 0
	global_load_lds_dwordx4 v166, s[22:23]
	s_mov_b32 m0, s1
	s_add_u32 s22, s24, 0x40000
	s_addc_u32 s23, s25, 0
	s_add_u32 s58, s24, 0x60000
	s_addc_u32 s59, s25, 0
	s_mov_b32 s1, m0
	s_mov_b32 m0, s42
	s_nop 0
	global_load_lds_dwordx4 v166, s[22:23]
	s_mov_b32 m0, s43
	s_nop 0
	global_load_lds_dwordx4 v166, s[58:59]
	s_mov_b32 m0, s1
	s_add_u32 s22, s31, s17
	s_addc_u32 s23, s34, s15
	s_add_u32 s58, s22, 0x20000
	s_addc_u32 s59, s23, 0
	s_mov_b32 s1, m0
	s_mov_b32 m0, s37
	s_nop 0
	global_load_lds_dwordx4 v167, s[22:23]
	s_mov_b32 m0, s44
	s_nop 0
	global_load_lds_dwordx4 v167, s[58:59]
	s_mov_b32 m0, s1
	s_waitcnt vmcnt(8)
	s_waitcnt lgkmcnt(0)
	s_setprio 1
	s_barrier
	s_waitcnt lgkmcnt(6)
	v_mfma_f32_16x16x128_f8f6f4 v[94:97], v[26:33], v[180:187], v[94:97]
	v_mfma_f32_16x16x128_f8f6f4 v[90:93], v[18:25], v[180:187], v[90:93]
	s_waitcnt lgkmcnt(4)
	v_mfma_f32_16x16x128_f8f6f4 v[86:89], v[26:33], v[188:195], v[86:89]
	v_mfma_f32_16x16x128_f8f6f4 v[82:85], v[18:25], v[188:195], v[82:85]
	s_waitcnt lgkmcnt(2)
	v_mfma_f32_16x16x128_f8f6f4 v[78:81], v[26:33], v[196:203], v[78:81]
	v_mfma_f32_16x16x128_f8f6f4 v[74:77], v[18:25], v[196:203], v[74:77]
	s_waitcnt lgkmcnt(0)
	v_mfma_f32_16x16x128_f8f6f4 v[70:73], v[26:33], v[204:211], v[70:73]
	v_mfma_f32_16x16x128_f8f6f4 v[66:69], v[18:25], v[204:211], v[66:69]
	s_setprio 0
	s_setprio 1
	v_mfma_f32_16x16x128_f8f6f4 v[62:65], v[10:17], v[180:187], v[62:65]
	v_mfma_f32_16x16x128_f8f6f4 v[58:61], v[2:9], v[180:187], v[58:61]
	v_mfma_f32_16x16x128_f8f6f4 v[54:57], v[10:17], v[188:195], v[54:57]
	v_mfma_f32_16x16x128_f8f6f4 v[50:53], v[2:9], v[188:195], v[50:53]
	v_mfma_f32_16x16x128_f8f6f4 v[46:49], v[10:17], v[196:203], v[46:49]
	v_mfma_f32_16x16x128_f8f6f4 v[42:45], v[2:9], v[196:203], v[42:45]
	v_mfma_f32_16x16x128_f8f6f4 v[38:41], v[10:17], v[204:211], v[38:41]
	v_mfma_f32_16x16x128_f8f6f4 v[34:37], v[2:9], v[204:211], v[34:37]
	s_setprio 0
	s_barrier
	ds_read_b128 v[26:29], v175
	ds_read_b128 v[30:33], v175 offset:1024
	ds_read_b128 v[18:21], v175 offset:2048
	ds_read_b128 v[22:25], v175 offset:3072
	ds_read_b128 v[10:13], v176
	ds_read_b128 v[14:17], v176 offset:1024
	ds_read_b128 v[2:5], v176 offset:2048
	ds_read_b128 v[6:9], v176 offset:3072
	ds_read_b128 v[180:183], v174 offset:32768
	ds_read_b128 v[184:187], v174 offset:33792
	ds_read_b128 v[188:191], v174 offset:34816
	ds_read_b128 v[192:195], v174 offset:35840
	ds_read_b128 v[196:199], v174 offset:36864
	ds_read_b128 v[200:203], v174 offset:37888
	ds_read_b128 v[204:207], v174 offset:38912
	ds_read_b128 v[208:211], v174 offset:39936
	s_add_u32 s58, s22, 0x40000
	s_addc_u32 s59, s23, 0
	s_add_u32 s60, s22, 0x60000
	s_addc_u32 s61, s23, 0
	s_mov_b32 s1, m0
	s_mov_b32 m0, s45
	s_nop 0
	global_load_lds_dwordx4 v167, s[58:59]
	s_mov_b32 m0, s46
	s_nop 0
	global_load_lds_dwordx4 v167, s[60:61]
	s_mov_b32 m0, s1
	s_waitcnt vmcnt(8)
	s_waitcnt lgkmcnt(0)
	s_setprio 1
	s_barrier
; #define PG8_STAGEB(bufoff, gbase) glds2(voffB, (gbase), voffB, (gbase) + qstep, ldsb + (bufoff))
; #define PG8_STAGEA(bufoff, rowb, v, h, kb) do { if constexpr (GATHER) glds2((v)[h][0], Ab + (kb), (v)[h][1], Ab + (kb), ldsb + (bufoff)); \
;         else glds2(voffA, Ab + (rowb) + (h) * hstep + (kb), voffA, Ab + (rowb) + (h) * hstep + qstep + (kb), ldsb + (bufoff)); } while (0)
; #define PG8_LDA(dst, b, h) do { _Pragma("unroll") for (int m = 0; m < 4; ++m) _Pragma("unroll") for (int k = 0; k < 2; ++k) dst[m][k] = *(const PG8_LAS bf16x8*)(lds + PG8_SA(b, h) + aoff + m * 2048 + k * 1024); } while (0)
; #define PG8_WAIT_V(n) asm volatile("s_waitcnt vmcnt(" #n ")" ::: "memory")
; #define PG8_WAIT_L(n) asm volatile("s_waitcnt lgkmcnt(" #n ")" ::: "memory")
; #define PG8_BAR __builtin_amdgcn_s_barrier()
; #define PG8_SCHED __builtin_amdgcn_sched_barrier(0)
; template <class Epi, bool GATHER, int MODE, bool SPLIT = false>
; __device__ __forceinline__ void gemm_phase(PG8_LAS unsigned char* lds, const Gemm g, const Order& S, const Epi& E) {
;     ...
;             PG8_LDA(At, 1, 1); PG8_STAGEB(PG8_SB(1, 0), nB + kstep); PG8_STAGEB(PG8_SB(1, 1), nB + hstep + kstep); PG8_STAGEA(PG8_SA(1, 0), nAr, nv, 0, kstep);
;             PG8_WAIT_V(8); PG8_WAIT_L(0); PG8_BAR; PG8_MMA(1, 0, At, B0); PG8_MMA(1, 1, At, B1); PG8_BAR; PG8_SCHED;
;         }
;         if (wr == 0) PG8_BAR;
	s_waitcnt lgkmcnt(6)
	v_mfma_f32_16x16x128_f8f6f4 v[158:161], v[26:33], v[180:187], v[158:161]
	v_mfma_f32_16x16x128_f8f6f4 v[154:157], v[18:25], v[180:187], v[154:157]
	s_waitcnt lgkmcnt(4)
	v_mfma_f32_16x16x128_f8f6f4 v[150:153], v[26:33], v[188:195], v[150:153]
	v_mfma_f32_16x16x128_f8f6f4 v[146:149], v[18:25], v[188:195], v[146:149]
	s_waitcnt lgkmcnt(2)
	v_mfma_f32_16x16x128_f8f6f4 v[142:145], v[26:33], v[196:203], v[142:145]
	v_mfma_f32_16x16x128_f8f6f4 v[138:141], v[18:25], v[196:203], v[138:141]
	s_waitcnt lgkmcnt(0)
	v_mfma_f32_16x16x128_f8f6f4 v[134:137], v[26:33], v[204:211], v[134:137]
	v_mfma_f32_16x16x128_f8f6f4 v[130:133], v[18:25], v[204:211], v[130:133]
	s_setprio 0
	s_setprio 1
	v_mfma_f32_16x16x128_f8f6f4 v[126:129], v[10:17], v[180:187], v[126:129]
	v_mfma_f32_16x16x128_f8f6f4 v[122:125], v[2:9], v[180:187], v[122:125]
	v_mfma_f32_16x16x128_f8f6f4 v[118:121], v[10:17], v[188:195], v[118:121]
	v_mfma_f32_16x16x128_f8f6f4 v[114:117], v[2:9], v[188:195], v[114:117]
	v_mfma_f32_16x16x128_f8f6f4 v[110:113], v[10:17], v[196:203], v[110:113]
	v_mfma_f32_16x16x128_f8f6f4 v[106:109], v[2:9], v[196:203], v[106:109]
	v_mfma_f32_16x16x128_f8f6f4 v[102:105], v[10:17], v[204:211], v[102:105]
	v_mfma_f32_16x16x128_f8f6f4 v[98:101], v[2:9], v[204:211], v[98:101]
	s_setprio 0
	s_barrier
	s_add_u32 s58, s24, 0x80
	s_addc_u32 s59, s25, 0
	s_add_u32 s60, s24, 0x20080
	s_addc_u32 s61, s25, 0
	ds_read_b128 v[180:183], v174 offset:49152
	ds_read_b128 v[184:187], v174 offset:50176
	ds_read_b128 v[188:191], v174 offset:51200
	ds_read_b128 v[192:195], v174 offset:52224
	ds_read_b128 v[196:199], v174 offset:53248
	ds_read_b128 v[200:203], v174 offset:54272
	ds_read_b128 v[204:207], v174 offset:55296
	ds_read_b128 v[208:211], v174 offset:56320
	s_mov_b32 s1, m0
	s_mov_b32 m0, s47
	s_nop 0
	global_load_lds_dwordx4 v166, s[58:59]
	s_mov_b32 m0, s48
	s_nop 0
	global_load_lds_dwordx4 v166, s[60:61]
	s_mov_b32 m0, s1
	s_add_u32 s58, s24, 0x40080
	s_addc_u32 s59, s25, 0
	s_add_u32 s24, s24, 0x60080
	s_addc_u32 s25, s25, 0
	s_mov_b32 s1, m0
	s_mov_b32 m0, s51
	s_nop 0
	global_load_lds_dwordx4 v166, s[58:59]
	s_mov_b32 m0, s52
	s_nop 0
	global_load_lds_dwordx4 v166, s[24:25]
	s_mov_b32 m0, s1
	s_add_u32 s24, s22, 0x80
	s_addc_u32 s25, s23, 0
	s_add_u32 s22, s22, 0x20080
	s_addc_u32 s23, s23, 0
	s_mov_b32 s1, m0
	s_mov_b32 m0, s49
	s_nop 0
	global_load_lds_dwordx4 v167, s[24:25]
	s_mov_b32 m0, s50
	s_nop 0
	global_load_lds_dwordx4 v167, s[22:23]
	s_mov_b32 m0, s1
	s_waitcnt vmcnt(8)
	s_waitcnt lgkmcnt(0)
	s_setprio 1
	s_barrier
	s_waitcnt lgkmcnt(6)
	v_mfma_f32_16x16x128_f8f6f4 v[94:97], v[26:33], v[180:187], v[94:97]
	v_mfma_f32_16x16x128_f8f6f4 v[90:93], v[18:25], v[180:187], v[90:93]
	s_waitcnt lgkmcnt(4)
	v_mfma_f32_16x16x128_f8f6f4 v[86:89], v[26:33], v[188:195], v[86:89]
	v_mfma_f32_16x16x128_f8f6f4 v[82:85], v[18:25], v[188:195], v[82:85]
	s_waitcnt lgkmcnt(2)
	v_mfma_f32_16x16x128_f8f6f4 v[78:81], v[26:33], v[196:203], v[78:81]
	v_mfma_f32_16x16x128_f8f6f4 v[74:77], v[18:25], v[196:203], v[74:77]
	s_waitcnt lgkmcnt(0)
	v_mfma_f32_16x16x128_f8f6f4 v[70:73], v[26:33], v[204:211], v[70:73]
	v_mfma_f32_16x16x128_f8f6f4 v[66:69], v[18:25], v[204:211], v[66:69]
	s_setprio 0
	s_setprio 1
	v_mfma_f32_16x16x128_f8f6f4 v[62:65], v[10:17], v[180:187], v[62:65]
	v_mfma_f32_16x16x128_f8f6f4 v[58:61], v[2:9], v[180:187], v[58:61]
	v_mfma_f32_16x16x128_f8f6f4 v[54:57], v[10:17], v[188:195], v[54:57]
	v_mfma_f32_16x16x128_f8f6f4 v[50:53], v[2:9], v[188:195], v[50:53]
	v_mfma_f32_16x16x128_f8f6f4 v[46:49], v[10:17], v[196:203], v[46:49]
	v_mfma_f32_16x16x128_f8f6f4 v[42:45], v[2:9], v[196:203], v[42:45]
	v_mfma_f32_16x16x128_f8f6f4 v[38:41], v[10:17], v[204:211], v[38:41]
	v_mfma_f32_16x16x128_f8f6f4 v[34:37], v[2:9], v[204:211], v[34:37]
	s_setprio 0
	s_nop 0
	s_andn2_b64 vcc, exec, s[8:9]
	s_cbranch_vccnz .LBB0_878
	s_barrier
